# baseline (speedup 1.0000x reference)
_Z16closed_form_mainPKfS0_PKiPf:
	s_load_dwordx8 s[16:23], s[0:1], 0x0
	s_lshr_b32 s6, s2, 3
	v_readfirstlane_b32 s0, v0
	s_mul_hi_u32 s7, s6, 0x24924925
	s_lshr_b32 s4, s0, 6
	s_and_b32 s0, s2, 7
	s_mul_i32 s1, s7, 7
	s_bfe_u32 s5, s2, 0x10003
	s_sub_i32 s1, s6, s1
	s_mul_i32 s36, s0, 7
	s_xor_b32 s3, s4, s5
	s_add_i32 s36, s36, s1
	s_waitcnt lgkmcnt(0)
	s_mov_b64 s[28:29], s[22:23]
	v_and_b32_e32 v19, 63, v0
	s_cmp_lt_u32 s36, 52
	s_mov_b64 s[0:1], -1
	s_cbranch_scc0 .LBB0_32
	s_mul_hi_u32 s0, s6, 0x20820821
	s_lshr_b32 s38, s0, 3
	s_mul_hi_u32 s0, s7, 0x1c71c71d
	s_mul_i32 s0, s0, 9
	s_sub_i32 s0, s7, s0
	v_add_u32_e32 v2, -3, v19
	v_mad_u64_u32 v[0:1], s[0:1], s0, 57, v[2:3]
	s_mov_b64 s[24:25], s[18:19]
	v_mov_b32_e32 v1, 0x200
	v_med3_i32 v1, v0, 0, v1
	s_mul_i32 s34, s36, 10
	s_and_b32 s17, s17, 0xffff
	s_and_b32 s25, s25, 0xffff
	v_cmp_gt_u32_e64 s[0:1], 57, v2
	s_mov_b32 s19, 0x20000
	s_mov_b32 s18, 0xe0e038
	s_mov_b32 s26, 0x606018
	s_mul_i32 s35, s38, 0x70701c
	s_mul_i32 s33, s38, 0x30300c
	v_lshlrev_b32_e32 v28, 2, v1
	v_mul_u32_u24_e32 v27, 12, v1
	v_lshlrev_b32_e32 v23, 4, v19
	s_cmp_lg_u32 s4, s5
	v_sub_u32_e64 v29, s34, 2 clamp
	s_cbranch_scc0 .LBB0_15
	s_setprio 3
	s_mov_b32 s27, s19
	s_and_b32 s21, s21, 0xffff
	s_mov_b32 s22, 0x202008
	s_mov_b32 s23, s19
	s_mul_i32 s38, s38, 0x101004
	s_movk_i32 s37, 0x80
	v_add_u32_e32 v18, -1, v0
	s_movk_i32 s4, 0x201
	s_movk_i32 s5, 0x1ff
	v_cmp_gt_u32_e64 s[40:41], s4, v0
	v_cmp_gt_u32_e64 s[42:43], s5, v18
	v_mov_b32_e32 v18, 0x42c80000
	v_mov_b32_e32 v22, 0x3de38e39
	v_mov_b32_e32 v26, 0x3a3d6628
	v_mov_b32_e32 v1, 0
	s_add_i32 s4, s34, -3
	s_max_i32 s4, s4, 0
	s_mul_i32 s4, s4, 0x804
	s_add_i32 s4, s4, s38
	buffer_load_dword v29, v28, s[20:23], s4 offen nt
	s_add_i32 s4, s34, -2
	s_max_i32 s4, s4, 0
	s_mul_i32 s4, s4, 0x804
	s_add_i32 s4, s4, s38
	buffer_load_dword v2, v28, s[20:23], s4 offen nt
	s_add_i32 s5, s34, -2
	s_max_i32 s5, s5, 0
	s_mul_i32 s6, s5, 0x804
	s_add_i32 s6, s6, s35
	s_add_i32 s7, s6, 0x505014
	s_add_i32 s8, s6, 0x606018
	s_mul_i32 s9, s5, 0x180c
	s_add_i32 s9, s9, s33
	s_add_i32 s4, s34, -1
	s_max_i32 s4, s4, 0
	s_mul_i32 s4, s4, 0x804
	s_add_i32 s4, s4, s38
	buffer_load_dword v3, v28, s[20:23], s4 offen nt
	buffer_load_dwordx3 v[8:10], v27, s[24:27], s9 offen nt
	buffer_load_dword v4, v28, s[16:19], s7 offen nt
	buffer_load_dword v5, v28, s[16:19], s8 offen nt
	s_add_i32 s5, s34, -1
	s_max_i32 s5, s5, 0
	s_mul_i32 s6, s5, 0x804
	s_add_i32 s6, s6, s35
	s_add_i32 s7, s6, 0x505014
	s_add_i32 s8, s6, 0x606018
	s_mul_i32 s9, s5, 0x180c
	s_add_i32 s9, s9, s33
	s_add_i32 s4, s34, 0
	s_min_i32 s4, s4, 0x200
	s_mul_i32 s4, s4, 0x804
	s_add_i32 s4, s4, s38
	buffer_load_dword v16, v28, s[20:23], s4 offen nt
	buffer_load_dwordx3 v[12:14], v27, s[24:27], s9 offen nt
	buffer_load_dword v6, v28, s[16:19], s7 offen nt
	buffer_load_dword v7, v28, s[16:19], s8 offen nt
	s_waitcnt vmcnt(8)
	s_add_i32 s4, s34, -3
	s_cmpk_lt_u32 s4, 0x201
	s_cselect_b64 s[12:13], s[40:41], 0
	v_cmp_eq_u32_e64 s[14:15], s37, v29
	s_and_b64 s[14:15], s[14:15], s[12:13]
	v_cndmask_b32_e64 v17, 0, 1, s[14:15]
	s_add_i32 s4, s34, -2
	s_cmpk_lt_u32 s4, 0x201
	s_cselect_b64 s[12:13], s[40:41], 0
	v_cmp_eq_u32_e64 s[14:15], s37, v2
	s_and_b64 s[14:15], s[14:15], s[12:13]
	v_cndmask_b32_e64 v20, 0, 1, s[14:15]
	s_nop 0
	v_or_b32_dpp v21, v17, v17 wave_shr:1 row_mask:0xf bank_mask:0xf bound_ctrl:1
	v_or_b32_dpp v24, v20, v20 wave_shr:1 row_mask:0xf bank_mask:0xf bound_ctrl:1
	s_nop 1
	v_or_b32_dpp v21, v17, v21 wave_shl:1 row_mask:0xf bank_mask:0xf bound_ctrl:1
	v_or_b32_dpp v24, v20, v24 wave_shl:1 row_mask:0xf bank_mask:0xf bound_ctrl:1
	s_nop 1
	v_or_b32_dpp v25, v21, v21 wave_shr:1 row_mask:0xf bank_mask:0xf bound_ctrl:1
	v_or_b32_dpp v30, v24, v24 wave_shr:1 row_mask:0xf bank_mask:0xf bound_ctrl:1
	s_nop 1
	v_or_b32_dpp v25, v21, v25 wave_shl:1 row_mask:0xf bank_mask:0xf bound_ctrl:1
	v_or_b32_dpp v30, v24, v30 wave_shl:1 row_mask:0xf bank_mask:0xf bound_ctrl:1
	v_mov_b32_e32 v17, 0
	v_mov_b32_e32 v24, 0
	s_add_i32 s5, s34, 0
	s_min_i32 s5, s5, 0x200
	s_mul_i32 s6, s5, 0x804
	s_add_i32 s6, s6, s35
	s_add_i32 s7, s6, 0x505014
	s_add_i32 s8, s6, 0x606018
	s_mul_i32 s9, s5, 0x180c
	s_add_i32 s9, s9, s33
	s_add_i32 s4, s34, 1
	s_min_i32 s4, s4, 0x200
	s_mul_i32 s4, s4, 0x804
	s_add_i32 s4, s4, s38
	buffer_load_dword v31, v28, s[20:23], s4 offen nt
	buffer_load_dwordx3 v[32:34], v27, s[24:27], s9 offen nt
	buffer_load_dword v20, v28, s[16:19], s7 offen nt
	buffer_load_dword v21, v28, s[16:19], s8 offen nt
	s_waitcnt vmcnt(8)
	v_mov_b32_dpp v36, v8 wave_shr:1 row_mask:0xf bank_mask:0xf bound_ctrl:1
	v_mov_b32_dpp v37, v9 wave_shr:1 row_mask:0xf bank_mask:0xf bound_ctrl:1
	v_mov_b32_dpp v38, v10 wave_shr:1 row_mask:0xf bank_mask:0xf bound_ctrl:1
	v_mov_b32_dpp v40, v8 wave_shl:1 row_mask:0xf bank_mask:0xf bound_ctrl:1
	v_mov_b32_dpp v41, v9 wave_shl:1 row_mask:0xf bank_mask:0xf bound_ctrl:1
	v_mov_b32_dpp v42, v10 wave_shl:1 row_mask:0xf bank_mask:0xf bound_ctrl:1
	s_add_i32 s4, s34, -1
	s_cmpk_lt_u32 s4, 0x201
	s_cselect_b64 s[12:13], s[40:41], 0
	v_cmp_eq_u32_e64 s[14:15], s37, v3
	s_and_b64 s[14:15], s[14:15], s[12:13]
	v_cndmask_b32_e64 v44, 0, 1, s[14:15]
	v_mul_f32_e64 v46, v8, v8
	v_mul_f32_e64 v47, v8, v9
	v_mul_f32_e64 v48, v8, v10
	v_mul_f32_e64 v49, v9, v9
	v_mul_f32_e64 v50, v9, v10
	v_mul_f32_e64 v51, v10, v10
	v_or_b32_dpp v45, v44, v44 wave_shr:1 row_mask:0xf bank_mask:0xf bound_ctrl:1
	s_nop 1
	v_or_b32_dpp v45, v44, v45 wave_shl:1 row_mask:0xf bank_mask:0xf bound_ctrl:1
	s_nop 1
	v_or_b32_dpp v52, v45, v45 wave_shr:1 row_mask:0xf bank_mask:0xf bound_ctrl:1
	s_nop 1
	v_or_b32_dpp v52, v45, v52 wave_shl:1 row_mask:0xf bank_mask:0xf bound_ctrl:1
	v_or3_b32 v53, v52, v30, v25
	v_or3_b32 v53, v53, v17, v24
	s_add_i32 s4, s34, -4
	s_cmpk_lt_u32 s4, 0x1ff
	s_cselect_b64 s[12:13], s[42:43], 0
	v_cmp_ne_u32_e64 s[30:31], 0, v53
	s_and_b64 s[30:31], s[30:31], s[12:13]
	v_cndmask_b32_e64 v53, 0, 1.0, s[30:31]
	v_add_f32_e64 v44, v8, v36
	v_add_f32_e64 v45, v9, v37
	v_add_f32_e64 v54, v10, v38
	v_fma_f32 v46, v36, v36, v46
	v_fma_f32 v47, v36, v37, v47
	v_fma_f32 v48, v36, v38, v48
	v_fma_f32 v49, v37, v37, v49
	v_fma_f32 v50, v37, v38, v50
	v_fma_f32 v51, v38, v38, v51
	v_add_f32_dpp v61, v53, v53 wave_shr:1 row_mask:0xf bank_mask:0xf bound_ctrl:1
	v_add_f32_e64 v44, v44, v40
	v_add_f32_e64 v45, v45, v41
	v_add_f32_e64 v54, v54, v42
	v_fma_f32 v55, v40, v40, v46
	v_fma_f32 v56, v40, v41, v47
	v_fma_f32 v57, v40, v42, v48
	v_fma_f32 v58, v41, v41, v49
	v_fma_f32 v59, v41, v42, v50
	v_fma_f32 v60, v42, v42, v51
	v_add_f32_dpp v61, v53, v61 wave_shl:1 row_mask:0xf bank_mask:0xf bound_ctrl:1
	s_barrier
	v_mov_b32_dpp v46, v4 wave_shr:1 row_mask:0xf bank_mask:0xf bound_ctrl:1
	v_mov_b32_dpp v47, v5 wave_shr:1 row_mask:0xf bank_mask:0xf bound_ctrl:1
	v_mov_b32_dpp v48, v4 wave_shl:1 row_mask:0xf bank_mask:0xf bound_ctrl:1
	v_mov_b32_dpp v49, v5 wave_shl:1 row_mask:0xf bank_mask:0xf bound_ctrl:1
	v_pk_mul_f32 v[50:51], v[4:5], v[8:9] op_sel_hi:[1,0]
	v_pk_mul_f32 v[62:63], v[4:5], v[8:9] op_sel:[0,1]
	v_pk_mul_f32 v[64:65], v[4:5], v[10:11] op_sel_hi:[1,0]
	v_pk_add_f32 v[66:67], v[4:5], v[46:47]
	v_pk_fma_f32 v[50:51], v[46:47], v[36:37], v[50:51] op_sel_hi:[1,0,1]
	v_pk_fma_f32 v[62:63], v[46:47], v[36:37], v[62:63] op_sel:[0,1,0]
	v_pk_fma_f32 v[64:65], v[46:47], v[38:39], v[64:65] op_sel_hi:[1,0,1]
	v_pk_add_f32 v[66:67], v[66:67], v[48:49]
	v_pk_fma_f32 v[50:51], v[48:49], v[40:41], v[50:51] op_sel_hi:[1,0,1]
	v_pk_fma_f32 v[62:63], v[48:49], v[40:41], v[62:63] op_sel:[0,1,0]
	v_pk_fma_f32 v[64:65], v[48:49], v[42:43], v[64:65] op_sel_hi:[1,0,1]
	s_add_i32 s5, s34, 1
	s_min_i32 s5, s5, 0x200
	s_mul_i32 s6, s5, 0x804
	s_add_i32 s6, s6, s35
	s_add_i32 s7, s6, 0x505014
	s_add_i32 s8, s6, 0x606018
	s_mul_i32 s9, s5, 0x180c
	s_add_i32 s9, s9, s33
	s_add_i32 s4, s34, 2
	s_min_i32 s4, s4, 0x200
	s_mul_i32 s4, s4, 0x804
	s_add_i32 s4, s4, s38
	buffer_load_dword v24, v28, s[20:23], s4 offen nt
	buffer_load_dwordx3 v[68:70], v27, s[24:27], s9 offen nt
	buffer_load_dword v46, v28, s[16:19], s7 offen nt
	buffer_load_dword v47, v28, s[16:19], s8 offen nt
	s_waitcnt vmcnt(8)
	v_mov_b32_dpp v72, v12 wave_shr:1 row_mask:0xf bank_mask:0xf bound_ctrl:1
	v_mov_b32_dpp v73, v13 wave_shr:1 row_mask:0xf bank_mask:0xf bound_ctrl:1
	v_mov_b32_dpp v74, v14 wave_shr:1 row_mask:0xf bank_mask:0xf bound_ctrl:1
	v_mov_b32_dpp v76, v12 wave_shl:1 row_mask:0xf bank_mask:0xf bound_ctrl:1
	v_mov_b32_dpp v77, v13 wave_shl:1 row_mask:0xf bank_mask:0xf bound_ctrl:1
	v_mov_b32_dpp v78, v14 wave_shl:1 row_mask:0xf bank_mask:0xf bound_ctrl:1
	s_add_i32 s4, s34, 0
	s_cmpk_lt_u32 s4, 0x201
	s_cselect_b64 s[12:13], s[40:41], 0
	v_cmp_eq_u32_e64 s[14:15], s37, v16
	s_and_b64 s[14:15], s[14:15], s[12:13]
	v_cndmask_b32_e64 v53, 0, 1, s[14:15]
	v_mul_f32_e64 v48, v12, v12
	v_mul_f32_e64 v49, v12, v13
	v_mul_f32_e64 v80, v12, v14
	v_mul_f32_e64 v81, v13, v13
	v_mul_f32_e64 v82, v13, v14
	v_mul_f32_e64 v83, v14, v14
	v_or_b32_dpp v84, v53, v53 wave_shr:1 row_mask:0xf bank_mask:0xf bound_ctrl:1
	s_nop 1
	v_or_b32_dpp v84, v53, v84 wave_shl:1 row_mask:0xf bank_mask:0xf bound_ctrl:1
	s_nop 1
	v_or_b32_dpp v85, v84, v84 wave_shr:1 row_mask:0xf bank_mask:0xf bound_ctrl:1
	s_nop 1
	v_or_b32_dpp v85, v84, v85 wave_shl:1 row_mask:0xf bank_mask:0xf bound_ctrl:1
	v_or3_b32 v53, v85, v52, v30
	v_or3_b32 v53, v53, v25, v17
	s_add_i32 s4, s34, -3
	s_cmpk_lt_u32 s4, 0x1ff
	s_cselect_b64 s[12:13], s[42:43], 0
	v_cmp_ne_u32_e64 s[30:31], 0, v53
	s_and_b64 s[30:31], s[30:31], s[12:13]
	v_cndmask_b32_e64 v53, 0, 1.0, s[30:31]
	v_add_f32_e64 v86, v12, v72
	v_add_f32_e64 v87, v13, v73
	v_add_f32_e64 v88, v14, v74
	v_fma_f32 v48, v72, v72, v48
	v_fma_f32 v49, v72, v73, v49
	v_fma_f32 v80, v72, v74, v80
	v_fma_f32 v81, v73, v73, v81
	v_fma_f32 v82, v73, v74, v82
	v_fma_f32 v83, v74, v74, v83
	v_add_f32_dpp v95, v53, v53 wave_shr:1 row_mask:0xf bank_mask:0xf bound_ctrl:1
	v_add_f32_e64 v86, v86, v76
	v_add_f32_e64 v87, v87, v77
	v_add_f32_e64 v88, v88, v78
	v_fma_f32 v89, v76, v76, v48
	v_fma_f32 v90, v76, v77, v49
	v_fma_f32 v91, v76, v78, v80
	v_fma_f32 v92, v77, v77, v81
	v_fma_f32 v93, v77, v78, v82
	v_fma_f32 v94, v78, v78, v83
	v_add_f32_dpp v95, v53, v95 wave_shl:1 row_mask:0xf bank_mask:0xf bound_ctrl:1
	s_barrier
	v_mov_b32_dpp v48, v6 wave_shr:1 row_mask:0xf bank_mask:0xf bound_ctrl:1
	v_mov_b32_dpp v49, v7 wave_shr:1 row_mask:0xf bank_mask:0xf bound_ctrl:1
	v_mov_b32_dpp v80, v6 wave_shl:1 row_mask:0xf bank_mask:0xf bound_ctrl:1
	v_mov_b32_dpp v81, v7 wave_shl:1 row_mask:0xf bank_mask:0xf bound_ctrl:1
	v_pk_mul_f32 v[82:83], v[6:7], v[12:13] op_sel_hi:[1,0]
	v_pk_mul_f32 v[96:97], v[6:7], v[12:13] op_sel:[0,1]
	v_pk_mul_f32 v[98:99], v[6:7], v[14:15] op_sel_hi:[1,0]
	v_pk_add_f32 v[100:101], v[6:7], v[48:49]
	v_pk_fma_f32 v[82:83], v[48:49], v[72:73], v[82:83] op_sel_hi:[1,0,1]
	v_pk_fma_f32 v[96:97], v[48:49], v[72:73], v[96:97] op_sel:[0,1,0]
	v_pk_fma_f32 v[98:99], v[48:49], v[74:75], v[98:99] op_sel_hi:[1,0,1]
	v_pk_add_f32 v[100:101], v[100:101], v[80:81]
	v_pk_fma_f32 v[82:83], v[80:81], v[76:77], v[82:83] op_sel_hi:[1,0,1]
	v_pk_fma_f32 v[96:97], v[80:81], v[76:77], v[96:97] op_sel:[0,1,0]
	v_pk_fma_f32 v[98:99], v[80:81], v[78:79], v[98:99] op_sel_hi:[1,0,1]
	s_add_i32 s5, s34, 2
	s_min_i32 s5, s5, 0x200
	s_mul_i32 s6, s5, 0x804
	s_add_i32 s6, s6, s35
	s_add_i32 s7, s6, 0x505014
	s_add_i32 s8, s6, 0x606018
	s_mul_i32 s9, s5, 0x180c
	s_add_i32 s9, s9, s33
	s_add_i32 s4, s34, 3
	s_min_i32 s4, s4, 0x200
	s_mul_i32 s4, s4, 0x804
	s_add_i32 s4, s4, s38
	buffer_load_dword v17, v28, s[20:23], s4 offen nt
	buffer_load_dwordx3 v[104:106], v27, s[24:27], s9 offen nt
	buffer_load_dword v48, v28, s[16:19], s7 offen nt
	buffer_load_dword v49, v28, s[16:19], s8 offen nt
	s_waitcnt vmcnt(8)
	v_mov_b32_dpp v108, v32 wave_shr:1 row_mask:0xf bank_mask:0xf bound_ctrl:1
	v_mov_b32_dpp v109, v33 wave_shr:1 row_mask:0xf bank_mask:0xf bound_ctrl:1
	v_mov_b32_dpp v110, v34 wave_shr:1 row_mask:0xf bank_mask:0xf bound_ctrl:1
	v_mov_b32_dpp v112, v32 wave_shl:1 row_mask:0xf bank_mask:0xf bound_ctrl:1
	v_mov_b32_dpp v113, v33 wave_shl:1 row_mask:0xf bank_mask:0xf bound_ctrl:1
	v_mov_b32_dpp v114, v34 wave_shl:1 row_mask:0xf bank_mask:0xf bound_ctrl:1
	s_add_i32 s4, s34, 1
	s_cmpk_lt_u32 s4, 0x201
	s_cselect_b64 s[12:13], s[40:41], 0
	v_cmp_eq_u32_e64 s[14:15], s37, v31
	s_and_b64 s[14:15], s[14:15], s[12:13]
	v_cndmask_b32_e64 v29, 0, 1, s[14:15]
	v_mul_f32_e64 v80, v32, v32
	v_mul_f32_e64 v81, v32, v33
	v_mul_f32_e64 v102, v32, v34
	v_mul_f32_e64 v103, v33, v33
	v_mul_f32_e64 v116, v33, v34
	v_mul_f32_e64 v117, v34, v34
	v_or_b32_dpp v53, v29, v29 wave_shr:1 row_mask:0xf bank_mask:0xf bound_ctrl:1
	s_nop 1
	v_or_b32_dpp v53, v29, v53 wave_shl:1 row_mask:0xf bank_mask:0xf bound_ctrl:1
	s_nop 1
	v_or_b32_dpp v84, v53, v53 wave_shr:1 row_mask:0xf bank_mask:0xf bound_ctrl:1
	s_nop 1
	v_or_b32_dpp v84, v53, v84 wave_shl:1 row_mask:0xf bank_mask:0xf bound_ctrl:1
	v_or3_b32 v29, v84, v85, v52
	v_or3_b32 v29, v29, v30, v25
	s_add_i32 s4, s34, -2
	s_cmpk_lt_u32 s4, 0x1ff
	s_cselect_b64 s[12:13], s[42:43], 0
	v_cmp_ne_u32_e64 s[30:31], 0, v29
	s_and_b64 s[30:31], s[30:31], s[12:13]
	v_cndmask_b32_e64 v29, 0, 1.0, s[30:31]
	v_add_f32_e64 v118, v32, v108
	v_add_f32_e64 v119, v33, v109
	v_add_f32_e64 v120, v34, v110
	v_fma_f32 v80, v108, v108, v80
	v_fma_f32 v81, v108, v109, v81
	v_fma_f32 v102, v108, v110, v102
	v_fma_f32 v103, v109, v109, v103
	v_fma_f32 v116, v109, v110, v116
	v_fma_f32 v117, v110, v110, v117
	v_add_f32_dpp v127, v29, v29 wave_shr:1 row_mask:0xf bank_mask:0xf bound_ctrl:1
	v_add_f32_e64 v118, v118, v112
	v_add_f32_e64 v119, v119, v113
	v_add_f32_e64 v120, v120, v114
	v_fma_f32 v121, v112, v112, v80
	v_fma_f32 v122, v112, v113, v81
	v_fma_f32 v123, v112, v114, v102
	v_fma_f32 v124, v113, v113, v103
	v_fma_f32 v125, v113, v114, v116
	v_fma_f32 v126, v114, v114, v117
	v_add_f32_dpp v127, v29, v127 wave_shl:1 row_mask:0xf bank_mask:0xf bound_ctrl:1
	v_pk_add_f32 v[80:81], v[86:87], v[118:119]
	v_pk_add_f32 v[102:103], v[44:45], v[80:81]
	v_pk_add_f32 v[44:45], v[88:89], v[120:121]
	v_pk_add_f32 v[86:87], v[54:55], v[44:45]
	v_pk_add_f32 v[54:55], v[90:91], v[122:123]
	v_pk_add_f32 v[88:89], v[56:57], v[54:55]
	v_pk_add_f32 v[56:57], v[92:93], v[124:125]
	v_pk_add_f32 v[90:91], v[58:59], v[56:57]
	v_pk_add_f32 v[58:59], v[94:95], v[126:127]
	v_pk_add_f32 v[92:93], v[60:61], v[58:59]
	v_mul_f32_e64 v128, v102, v22
	v_mul_f32_e64 v129, v103, v22
	v_mul_f32_e64 v130, v86, v22
	v_fma_f32 v29, v87, v22, v26
	v_mul_f32_e64 v53, v88, v22
	v_mul_f32_e64 v60, v89, v22
	v_fma_f32 v61, v90, v22, v26
	v_mul_f32_e64 v94, v91, v22
	v_fma_f32 v95, v92, v22, v26
	v_fma_f32 v29, -v128, v128, v29
	v_fma_f32 v53, -v128, v129, v53
	v_fma_f32 v60, -v128, v130, v60
	v_fma_f32 v61, -v129, v129, v61
	v_fma_f32 v94, -v129, v130, v94
	v_fma_f32 v95, -v130, v130, v95
	v_mul_f32_e64 v116, v94, v94
	v_mul_f32_e64 v117, v53, v95
	v_mul_f32_e64 v140, v60, v61
	v_mul_f32_e64 v141, v60, v60
	v_mul_f32_e64 v142, v29, v94
	v_mul_f32_e64 v143, v53, v53
	v_fma_f32 v116, v61, v95, -v116
	v_fma_f32 v117, v60, v94, -v117
	v_fma_f32 v140, v53, v94, -v140
	v_fma_f32 v141, v29, v95, -v141
	v_fma_f32 v142, v53, v60, -v142
	v_fma_f32 v143, v29, v61, -v143
	v_mul_f32_e64 v144, v29, v116
	v_fma_f32 v144, v53, v117, v144
	v_fma_f32 v144, v60, v140, v144
	v_rcp_f32_e32 v144, v144
	v_cmp_ne_u32_e64 vcc, s37, v2
	v_mul_f32_e64 v144, v144, v22
	v_cndmask_b32_e64 v144, 0, v144, s[30:31]
	v_cndmask_b32_e64 v29, 0, v18, vcc
	v_cndmask_b32_e64 v137, 0, v22, s[30:31]
	v_mul_f32_e64 v131, v116, v144
	v_mul_f32_e64 v132, v117, v144
	v_mul_f32_e64 v133, v140, v144
	v_mul_f32_e64 v134, v141, v144
	v_mul_f32_e64 v135, v142, v144
	v_mul_f32_e64 v136, v143, v144
	v_add_f32_e64 v138, v93, v29
	v_mov_b32_e32 v139, v2
	ds_write_b128 v23, v[128:131]
	ds_write_b128 v23, v[132:135] offset:1024
	ds_write_b128 v23, v[136:139] offset:2048
	s_waitcnt lgkmcnt(0)
	s_barrier
	v_mov_b32_dpp v60, v20 wave_shr:1 row_mask:0xf bank_mask:0xf bound_ctrl:1
	v_mov_b32_dpp v61, v21 wave_shr:1 row_mask:0xf bank_mask:0xf bound_ctrl:1
	v_mov_b32_dpp v86, v20 wave_shl:1 row_mask:0xf bank_mask:0xf bound_ctrl:1
	v_mov_b32_dpp v87, v21 wave_shl:1 row_mask:0xf bank_mask:0xf bound_ctrl:1
	v_pk_mul_f32 v[88:89], v[20:21], v[32:33] op_sel_hi:[1,0]
	v_pk_mul_f32 v[90:91], v[20:21], v[32:33] op_sel:[0,1]
	v_pk_mul_f32 v[92:93], v[20:21], v[34:35] op_sel_hi:[1,0]
	v_pk_add_f32 v[94:95], v[20:21], v[60:61]
	v_pk_fma_f32 v[88:89], v[60:61], v[108:109], v[88:89] op_sel_hi:[1,0,1]
	v_pk_fma_f32 v[90:91], v[60:61], v[108:109], v[90:91] op_sel:[0,1,0]
	v_pk_fma_f32 v[92:93], v[60:61], v[110:111], v[92:93] op_sel_hi:[1,0,1]
	v_pk_add_f32 v[94:95], v[94:95], v[86:87]
	v_pk_fma_f32 v[88:89], v[86:87], v[112:113], v[88:89] op_sel_hi:[1,0,1]
	v_pk_fma_f32 v[90:91], v[86:87], v[112:113], v[90:91] op_sel:[0,1,0]
	v_pk_fma_f32 v[92:93], v[86:87], v[114:115], v[92:93] op_sel_hi:[1,0,1]
	v_pk_add_f32 v[60:61], v[100:101], v[94:95]
	v_pk_add_f32 v[86:87], v[66:67], v[60:61]
	v_pk_add_f32 v[66:67], v[82:83], v[88:89]
	v_pk_add_f32 v[100:101], v[50:51], v[66:67]
	v_pk_add_f32 v[50:51], v[96:97], v[90:91]
	v_pk_add_f32 v[82:83], v[62:63], v[50:51]
	v_pk_add_f32 v[62:63], v[98:99], v[92:93]
	v_pk_add_f32 v[96:97], v[64:65], v[62:63]
	v_pk_fma_f32 v[100:101], v[128:129], v[86:87], v[100:101] op_sel_hi:[0,1,1] neg_lo:[1,0,0] neg_hi:[1,0,0]
	v_pk_fma_f32 v[82:83], v[128:129], v[86:87], v[82:83] op_sel:[1,0,0] neg_lo:[1,0,0] neg_hi:[1,0,0]
	v_pk_fma_f32 v[96:97], v[130:131], v[86:87], v[96:97] op_sel_hi:[0,1,1] neg_lo:[1,0,0] neg_hi:[1,0,0]
	v_pk_mul_f32 v[64:65], v[130:131], v[100:101] op_sel:[1,0]
	v_pk_mul_f32 v[98:99], v[132:133], v[100:101] op_sel_hi:[0,1]
	v_pk_mul_f32 v[102:103], v[132:133], v[100:101] op_sel:[1,0]
	v_pk_fma_f32 v[64:65], v[132:133], v[82:83], v[64:65] op_sel_hi:[0,1,1]
	v_pk_fma_f32 v[98:99], v[134:135], v[82:83], v[98:99] op_sel_hi:[0,1,1]
	v_pk_fma_f32 v[102:103], v[134:135], v[82:83], v[102:103] op_sel:[1,0,0]
	v_pk_fma_f32 v[64:65], v[132:133], v[96:97], v[64:65] op_sel:[1,0,0]
	v_pk_fma_f32 v[98:99], v[134:135], v[96:97], v[98:99] op_sel:[1,0,0]
	v_pk_fma_f32 v[102:103], v[136:137], v[96:97], v[102:103] op_sel_hi:[0,1,1]
	v_pk_mul_f32 v[116:117], v[128:129], v[64:65] op_sel_hi:[0,1]
	v_pk_fma_f32 v[116:117], v[128:129], v[98:99], v[116:117] op_sel:[1,0,0]
	v_pk_fma_f32 v[116:117], v[130:131], v[102:103], v[116:117] op_sel_hi:[0,1,1]
	v_pk_fma_f32 v[116:117], v[136:137], v[86:87], v[116:117] op_sel:[1,0,0] neg_lo:[0,0,1] neg_hi:[0,0,1]
	s_add_i32 s5, s34, 3
	s_min_i32 s5, s5, 0x200
	s_mul_i32 s6, s5, 0x804
	s_add_i32 s6, s6, s35
	s_add_i32 s7, s6, 0x505014
	s_add_i32 s8, s6, 0x606018
	s_mul_i32 s9, s5, 0x180c
	s_add_i32 s9, s9, s33
	s_add_i32 s4, s34, 4
	s_min_i32 s4, s4, 0x200
	s_mul_i32 s4, s4, 0x804
	s_add_i32 s4, s4, s38
	buffer_load_dword v2, v28, s[20:23], s4 offen nt
	buffer_load_dwordx3 v[8:10], v27, s[24:27], s9 offen nt
	buffer_load_dword v4, v28, s[16:19], s7 offen nt
	buffer_load_dword v5, v28, s[16:19], s8 offen nt
	s_waitcnt vmcnt(8)
	v_mov_b32_dpp v36, v68 wave_shr:1 row_mask:0xf bank_mask:0xf bound_ctrl:1
	v_mov_b32_dpp v37, v69 wave_shr:1 row_mask:0xf bank_mask:0xf bound_ctrl:1
	v_mov_b32_dpp v38, v70 wave_shr:1 row_mask:0xf bank_mask:0xf bound_ctrl:1
	v_mov_b32_dpp v40, v68 wave_shl:1 row_mask:0xf bank_mask:0xf bound_ctrl:1
	v_mov_b32_dpp v41, v69 wave_shl:1 row_mask:0xf bank_mask:0xf bound_ctrl:1
	v_mov_b32_dpp v42, v70 wave_shl:1 row_mask:0xf bank_mask:0xf bound_ctrl:1
	s_add_i32 s4, s34, 2
	s_cmpk_lt_u32 s4, 0x201
	s_cselect_b64 s[12:13], s[40:41], 0
	v_cmp_eq_u32_e64 s[14:15], s37, v24
	s_and_b64 s[14:15], s[14:15], s[12:13]
	v_cndmask_b32_e64 v25, 0, 1, s[14:15]
	v_mul_f32_e64 v82, v68, v68
	v_mul_f32_e64 v83, v68, v69
	v_mul_f32_e64 v86, v68, v70
	v_mul_f32_e64 v87, v69, v69
	v_mul_f32_e64 v96, v69, v70
	v_mul_f32_e64 v97, v70, v70
	v_or_b32_dpp v29, v25, v25 wave_shr:1 row_mask:0xf bank_mask:0xf bound_ctrl:1
	s_nop 1
	v_or_b32_dpp v29, v25, v29 wave_shl:1 row_mask:0xf bank_mask:0xf bound_ctrl:1
	s_nop 1
	v_or_b32_dpp v53, v29, v29 wave_shr:1 row_mask:0xf bank_mask:0xf bound_ctrl:1
	s_nop 1
	v_or_b32_dpp v53, v29, v53 wave_shl:1 row_mask:0xf bank_mask:0xf bound_ctrl:1
	v_or3_b32 v25, v53, v84, v85
	v_or3_b32 v25, v25, v52, v30
	s_add_i32 s4, s34, -1
	s_cmpk_lt_u32 s4, 0x1ff
	s_cselect_b64 s[12:13], s[42:43], 0
	v_cmp_ne_u32_e64 s[30:31], 0, v25
	s_and_b64 s[30:31], s[30:31], s[12:13]
	v_cndmask_b32_e64 v25, 0, 1.0, s[30:31]
	v_add_f32_e64 v100, v68, v36
	v_add_f32_e64 v101, v69, v37
	v_add_f32_e64 v128, v70, v38
	v_fma_f32 v82, v36, v36, v82
	v_fma_f32 v83, v36, v37, v83
	v_fma_f32 v86, v36, v38, v86
	v_fma_f32 v87, v37, v37, v87
	v_fma_f32 v96, v37, v38, v96
	v_fma_f32 v97, v38, v38, v97
	v_add_f32_dpp v135, v25, v25 wave_shr:1 row_mask:0xf bank_mask:0xf bound_ctrl:1
	v_add_f32_e64 v100, v100, v40
	v_add_f32_e64 v101, v101, v41
	v_add_f32_e64 v128, v128, v42
	v_fma_f32 v129, v40, v40, v82
	v_fma_f32 v130, v40, v41, v83
	v_fma_f32 v131, v40, v42, v86
	v_fma_f32 v132, v41, v41, v87
	v_fma_f32 v133, v41, v42, v96
	v_fma_f32 v134, v42, v42, v97
	v_add_f32_dpp v135, v25, v135 wave_shl:1 row_mask:0xf bank_mask:0xf bound_ctrl:1
	v_pk_add_f32 v[82:83], v[80:81], v[100:101]
	v_pk_add_f32 v[80:81], v[44:45], v[128:129]
	v_pk_add_f32 v[44:45], v[54:55], v[130:131]
	v_pk_add_f32 v[54:55], v[56:57], v[132:133]
	v_pk_add_f32 v[56:57], v[58:59], v[134:135]
	v_mul_f32_e64 v136, v82, v22
	v_mul_f32_e64 v137, v83, v22
	v_mul_f32_e64 v138, v80, v22
	v_fma_f32 v25, v81, v22, v26
	v_mul_f32_e64 v29, v44, v22
	v_mul_f32_e64 v58, v45, v22
	v_fma_f32 v59, v54, v22, v26
	v_mul_f32_e64 v86, v55, v22
	v_fma_f32 v87, v56, v22, v26
	v_fma_f32 v25, -v136, v136, v25
	v_fma_f32 v29, -v136, v137, v29
	v_fma_f32 v58, -v136, v138, v58
	v_fma_f32 v59, -v137, v137, v59
	v_fma_f32 v86, -v137, v138, v86
	v_fma_f32 v87, -v138, v138, v87
	v_mul_f32_e64 v96, v86, v86
	v_mul_f32_e64 v97, v29, v87
	v_mul_f32_e64 v148, v58, v59
	v_mul_f32_e64 v149, v58, v58
	v_mul_f32_e64 v150, v25, v86
	v_mul_f32_e64 v151, v29, v29
	v_fma_f32 v96, v59, v87, -v96
	v_fma_f32 v97, v58, v86, -v97
	v_fma_f32 v148, v29, v86, -v148
	v_fma_f32 v149, v25, v87, -v149
	v_fma_f32 v150, v29, v58, -v150
	v_fma_f32 v151, v25, v59, -v151
	v_mul_f32_e64 v152, v25, v96
	v_fma_f32 v152, v29, v97, v152
	v_fma_f32 v152, v58, v148, v152
	v_rcp_f32_e32 v152, v152
	v_cmp_ne_u32_e64 vcc, s37, v3
	v_mul_f32_e64 v152, v152, v22
	v_cndmask_b32_e64 v152, 0, v152, s[30:31]
	v_cndmask_b32_e64 v25, 0, v18, vcc
	v_cndmask_b32_e64 v145, 0, v22, s[30:31]
	v_mul_f32_e64 v139, v96, v152
	v_mul_f32_e64 v140, v97, v152
	v_mul_f32_e64 v141, v148, v152
	v_mul_f32_e64 v142, v149, v152
	v_mul_f32_e64 v143, v150, v152
	v_mul_f32_e64 v144, v151, v152
	v_add_f32_e64 v146, v57, v25
	v_mov_b32_e32 v147, v3
	ds_write_b128 v23, v[136:139] offset:3072
	ds_write_b128 v23, v[140:143] offset:4096
	ds_write_b128 v23, v[144:147] offset:5120
	s_waitcnt lgkmcnt(0)
	s_barrier
	v_mov_b32_dpp v44, v46 wave_shr:1 row_mask:0xf bank_mask:0xf bound_ctrl:1
	v_mov_b32_dpp v45, v47 wave_shr:1 row_mask:0xf bank_mask:0xf bound_ctrl:1
	v_mov_b32_dpp v54, v46 wave_shl:1 row_mask:0xf bank_mask:0xf bound_ctrl:1
	v_mov_b32_dpp v55, v47 wave_shl:1 row_mask:0xf bank_mask:0xf bound_ctrl:1
	v_pk_mul_f32 v[56:57], v[46:47], v[68:69] op_sel_hi:[1,0]
	v_pk_mul_f32 v[58:59], v[46:47], v[68:69] op_sel:[0,1]
	v_pk_mul_f32 v[80:81], v[46:47], v[70:71] op_sel_hi:[1,0]
	v_pk_add_f32 v[82:83], v[46:47], v[44:45]
	v_pk_fma_f32 v[56:57], v[44:45], v[36:37], v[56:57] op_sel_hi:[1,0,1]
	v_pk_fma_f32 v[58:59], v[44:45], v[36:37], v[58:59] op_sel:[0,1,0]
	v_pk_fma_f32 v[80:81], v[44:45], v[38:39], v[80:81] op_sel_hi:[1,0,1]
	v_pk_add_f32 v[82:83], v[82:83], v[54:55]
	v_pk_fma_f32 v[56:57], v[54:55], v[40:41], v[56:57] op_sel_hi:[1,0,1]
	v_pk_fma_f32 v[58:59], v[54:55], v[40:41], v[58:59] op_sel:[0,1,0]
	v_pk_fma_f32 v[80:81], v[54:55], v[42:43], v[80:81] op_sel_hi:[1,0,1]
	v_pk_add_f32 v[44:45], v[60:61], v[82:83]
	v_pk_add_f32 v[54:55], v[66:67], v[56:57]
	v_pk_add_f32 v[60:61], v[50:51], v[58:59]
	v_pk_add_f32 v[50:51], v[62:63], v[80:81]
	v_pk_fma_f32 v[54:55], v[136:137], v[44:45], v[54:55] op_sel_hi:[0,1,1] neg_lo:[1,0,0] neg_hi:[1,0,0]
	v_pk_fma_f32 v[60:61], v[136:137], v[44:45], v[60:61] op_sel:[1,0,0] neg_lo:[1,0,0] neg_hi:[1,0,0]
	v_pk_fma_f32 v[50:51], v[138:139], v[44:45], v[50:51] op_sel_hi:[0,1,1] neg_lo:[1,0,0] neg_hi:[1,0,0]
	v_pk_mul_f32 v[62:63], v[138:139], v[54:55] op_sel:[1,0]
	v_pk_mul_f32 v[66:67], v[140:141], v[54:55] op_sel_hi:[0,1]
	v_pk_mul_f32 v[86:87], v[140:141], v[54:55] op_sel:[1,0]
	v_pk_fma_f32 v[62:63], v[140:141], v[60:61], v[62:63] op_sel_hi:[0,1,1]
	v_pk_fma_f32 v[66:67], v[142:143], v[60:61], v[66:67] op_sel_hi:[0,1,1]
	v_pk_fma_f32 v[86:87], v[142:143], v[60:61], v[86:87] op_sel:[1,0,0]
	v_pk_fma_f32 v[62:63], v[140:141], v[50:51], v[62:63] op_sel:[1,0,0]
	v_pk_fma_f32 v[66:67], v[142:143], v[50:51], v[66:67] op_sel:[1,0,0]
	v_pk_fma_f32 v[86:87], v[144:145], v[50:51], v[86:87] op_sel_hi:[0,1,1]
	v_pk_mul_f32 v[96:97], v[136:137], v[62:63] op_sel_hi:[0,1]
	v_pk_fma_f32 v[96:97], v[136:137], v[66:67], v[96:97] op_sel:[1,0,0]
	v_pk_fma_f32 v[96:97], v[138:139], v[86:87], v[96:97] op_sel_hi:[0,1,1]
	v_pk_fma_f32 v[96:97], v[144:145], v[44:45], v[96:97] op_sel:[1,0,0] neg_lo:[0,0,1] neg_hi:[0,0,1]
	s_add_i32 s5, s34, 4
	s_min_i32 s5, s5, 0x200
	s_mul_i32 s6, s5, 0x804
	s_add_i32 s6, s6, s35
	s_add_i32 s7, s6, 0x505014
	s_add_i32 s8, s6, 0x606018
	s_mul_i32 s9, s5, 0x180c
	s_add_i32 s9, s9, s33
	s_add_i32 s4, s34, 5
	s_min_i32 s4, s4, 0x200
	s_mul_i32 s4, s4, 0x804
	s_add_i32 s4, s4, s38
	buffer_load_dword v3, v28, s[20:23], s4 offen nt
	buffer_load_dwordx3 v[12:14], v27, s[24:27], s9 offen nt
	buffer_load_dword v6, v28, s[16:19], s7 offen nt
	buffer_load_dword v7, v28, s[16:19], s8 offen nt
	s_waitcnt vmcnt(8)
	v_mov_b32_dpp v72, v104 wave_shr:1 row_mask:0xf bank_mask:0xf bound_ctrl:1
	v_mov_b32_dpp v73, v105 wave_shr:1 row_mask:0xf bank_mask:0xf bound_ctrl:1
	v_mov_b32_dpp v74, v106 wave_shr:1 row_mask:0xf bank_mask:0xf bound_ctrl:1
	v_mov_b32_dpp v76, v104 wave_shl:1 row_mask:0xf bank_mask:0xf bound_ctrl:1
	v_mov_b32_dpp v77, v105 wave_shl:1 row_mask:0xf bank_mask:0xf bound_ctrl:1
	v_mov_b32_dpp v78, v106 wave_shl:1 row_mask:0xf bank_mask:0xf bound_ctrl:1
	s_add_i32 s4, s34, 3
	s_cmpk_lt_u32 s4, 0x201
	s_cselect_b64 s[12:13], s[40:41], 0
	v_cmp_eq_u32_e64 s[14:15], s37, v17
	s_and_b64 s[14:15], s[14:15], s[12:13]
	v_cndmask_b32_e64 v25, 0, 1, s[14:15]
	v_mul_f32_e64 v44, v104, v104
	v_mul_f32_e64 v45, v104, v105
	v_mul_f32_e64 v50, v104, v106
	v_mul_f32_e64 v51, v105, v105
	v_mul_f32_e64 v54, v105, v106
	v_mul_f32_e64 v55, v106, v106
	v_or_b32_dpp v29, v25, v25 wave_shr:1 row_mask:0xf bank_mask:0xf bound_ctrl:1
	s_nop 1
	v_or_b32_dpp v29, v25, v29 wave_shl:1 row_mask:0xf bank_mask:0xf bound_ctrl:1
	s_nop 1
	v_or_b32_dpp v30, v29, v29 wave_shr:1 row_mask:0xf bank_mask:0xf bound_ctrl:1
	s_nop 1
	v_or_b32_dpp v30, v29, v30 wave_shl:1 row_mask:0xf bank_mask:0xf bound_ctrl:1
	v_or3_b32 v25, v30, v53, v84
	v_or3_b32 v25, v25, v85, v52
	s_add_i32 s4, s34, 0
	s_cmpk_lt_u32 s4, 0x1ff
	s_cselect_b64 s[12:13], s[42:43], 0
	v_cmp_ne_u32_e64 s[30:31], 0, v25
	s_and_b64 s[30:31], s[30:31], s[12:13]
	v_cndmask_b32_e64 v25, 0, 1.0, s[30:31]
	v_add_f32_e64 v60, v104, v72
	v_add_f32_e64 v61, v105, v73
	v_add_f32_e64 v136, v106, v74
	v_fma_f32 v44, v72, v72, v44
	v_fma_f32 v45, v72, v73, v45
	v_fma_f32 v50, v72, v74, v50
	v_fma_f32 v51, v73, v73, v51
	v_fma_f32 v54, v73, v74, v54
	v_fma_f32 v55, v74, v74, v55
	v_add_f32_dpp v143, v25, v25 wave_shr:1 row_mask:0xf bank_mask:0xf bound_ctrl:1
	v_add_f32_e64 v60, v60, v76
	v_add_f32_e64 v61, v61, v77
	v_add_f32_e64 v136, v136, v78
	v_fma_f32 v137, v76, v76, v44
	v_fma_f32 v138, v76, v77, v45
	v_fma_f32 v139, v76, v78, v50
	v_fma_f32 v140, v77, v77, v51
	v_fma_f32 v141, v77, v78, v54
	v_fma_f32 v142, v78, v78, v55
	v_add_f32_dpp v143, v25, v143 wave_shl:1 row_mask:0xf bank_mask:0xf bound_ctrl:1
	v_pk_add_f32 v[44:45], v[100:101], v[60:61]
	v_pk_add_f32 v[50:51], v[118:119], v[44:45]
	v_pk_add_f32 v[54:55], v[128:129], v[136:137]
	v_pk_add_f32 v[100:101], v[120:121], v[54:55]
	v_pk_add_f32 v[118:119], v[130:131], v[138:139]
	v_pk_add_f32 v[120:121], v[122:123], v[118:119]
	v_pk_add_f32 v[122:123], v[132:133], v[140:141]
	v_pk_add_f32 v[128:129], v[124:125], v[122:123]
	v_pk_add_f32 v[124:125], v[134:135], v[142:143]
	v_pk_add_f32 v[130:131], v[126:127], v[124:125]
	v_mul_f32_e64 v132, v50, v22
	v_mul_f32_e64 v133, v51, v22
	v_mul_f32_e64 v134, v100, v22
	v_fma_f32 v25, v101, v22, v26
	v_mul_f32_e64 v29, v120, v22
	v_mul_f32_e64 v126, v121, v22
	v_fma_f32 v127, v128, v22, v26
	v_mul_f32_e64 v152, v129, v22
	v_fma_f32 v153, v130, v22, v26
	v_fma_f32 v25, -v132, v132, v25
	v_fma_f32 v29, -v132, v133, v29
	v_fma_f32 v126, -v132, v134, v126
	v_fma_f32 v127, -v133, v133, v127
	v_fma_f32 v152, -v133, v134, v152
	v_fma_f32 v153, -v134, v134, v153
	v_mul_f32_e64 v154, v152, v152
	v_mul_f32_e64 v155, v29, v153
	v_mul_f32_e64 v156, v126, v127
	v_mul_f32_e64 v157, v126, v126
	v_mul_f32_e64 v158, v25, v152
	v_mul_f32_e64 v159, v29, v29
	v_fma_f32 v154, v127, v153, -v154
	v_fma_f32 v155, v126, v152, -v155
	v_fma_f32 v156, v29, v152, -v156
	v_fma_f32 v157, v25, v153, -v157
	v_fma_f32 v158, v29, v126, -v158
	v_fma_f32 v159, v25, v127, -v159
	v_mul_f32_e64 v160, v25, v154
	v_fma_f32 v160, v29, v155, v160
	v_fma_f32 v160, v126, v156, v160
	v_rcp_f32_e32 v160, v160
	v_cmp_ne_u32_e64 vcc, s37, v16
	v_mul_f32_e64 v160, v160, v22
	v_cndmask_b32_e64 v160, 0, v160, s[30:31]
	v_cndmask_b32_e64 v25, 0, v18, vcc
	v_cndmask_b32_e64 v149, 0, v22, s[30:31]
	v_mul_f32_e64 v135, v154, v160
	v_mul_f32_e64 v144, v155, v160
	v_mul_f32_e64 v145, v156, v160
	v_mul_f32_e64 v146, v157, v160
	v_mul_f32_e64 v147, v158, v160
	v_mul_f32_e64 v148, v159, v160
	v_add_f32_e64 v150, v131, v25
	v_mov_b32_e32 v151, v16
	ds_write_b128 v23, v[132:135]
	ds_write_b128 v23, v[144:147] offset:1024
	ds_write_b128 v23, v[148:151] offset:2048
	s_waitcnt lgkmcnt(0)
	s_barrier
	v_mov_b32_dpp v50, v48 wave_shr:1 row_mask:0xf bank_mask:0xf bound_ctrl:1
	v_mov_b32_dpp v51, v49 wave_shr:1 row_mask:0xf bank_mask:0xf bound_ctrl:1
	v_mov_b32_dpp v100, v48 wave_shl:1 row_mask:0xf bank_mask:0xf bound_ctrl:1
	v_mov_b32_dpp v101, v49 wave_shl:1 row_mask:0xf bank_mask:0xf bound_ctrl:1
	v_pk_mul_f32 v[120:121], v[48:49], v[104:105] op_sel_hi:[1,0]
	v_pk_mul_f32 v[126:127], v[48:49], v[104:105] op_sel:[0,1]
	v_pk_mul_f32 v[128:129], v[48:49], v[106:107] op_sel_hi:[1,0]
	v_pk_add_f32 v[130:131], v[48:49], v[50:51]
	v_pk_fma_f32 v[120:121], v[50:51], v[72:73], v[120:121] op_sel_hi:[1,0,1]
	v_pk_fma_f32 v[126:127], v[50:51], v[72:73], v[126:127] op_sel:[0,1,0]
	v_pk_fma_f32 v[128:129], v[50:51], v[74:75], v[128:129] op_sel_hi:[1,0,1]
	v_pk_add_f32 v[130:131], v[130:131], v[100:101]
	v_pk_fma_f32 v[120:121], v[100:101], v[76:77], v[120:121] op_sel_hi:[1,0,1]
	v_pk_fma_f32 v[126:127], v[100:101], v[76:77], v[126:127] op_sel:[0,1,0]
	v_pk_fma_f32 v[128:129], v[100:101], v[78:79], v[128:129] op_sel_hi:[1,0,1]
	v_pk_add_f32 v[50:51], v[82:83], v[130:131]
	v_pk_add_f32 v[100:101], v[94:95], v[50:51]
	v_pk_add_f32 v[82:83], v[56:57], v[120:121]
	v_pk_add_f32 v[94:95], v[88:89], v[82:83]
	v_pk_add_f32 v[56:57], v[58:59], v[126:127]
	v_pk_add_f32 v[88:89], v[90:91], v[56:57]
	v_pk_add_f32 v[58:59], v[80:81], v[128:129]
	v_pk_add_f32 v[90:91], v[92:93], v[58:59]
	v_pk_fma_f32 v[94:95], v[132:133], v[100:101], v[94:95] op_sel_hi:[0,1,1] neg_lo:[1,0,0] neg_hi:[1,0,0]
	v_pk_fma_f32 v[88:89], v[132:133], v[100:101], v[88:89] op_sel:[1,0,0] neg_lo:[1,0,0] neg_hi:[1,0,0]
	v_pk_fma_f32 v[90:91], v[134:135], v[100:101], v[90:91] op_sel_hi:[0,1,1] neg_lo:[1,0,0] neg_hi:[1,0,0]
	v_pk_mul_f32 v[80:81], v[134:135], v[94:95] op_sel:[1,0]
	v_pk_mul_f32 v[92:93], v[144:145], v[94:95] op_sel_hi:[0,1]
	v_pk_mul_f32 v[152:153], v[144:145], v[94:95] op_sel:[1,0]
	v_pk_fma_f32 v[80:81], v[144:145], v[88:89], v[80:81] op_sel_hi:[0,1,1]
	v_pk_fma_f32 v[92:93], v[146:147], v[88:89], v[92:93] op_sel_hi:[0,1,1]
	v_pk_fma_f32 v[152:153], v[146:147], v[88:89], v[152:153] op_sel:[1,0,0]
	v_pk_fma_f32 v[80:81], v[144:145], v[90:91], v[80:81] op_sel:[1,0,0]
	v_pk_fma_f32 v[92:93], v[146:147], v[90:91], v[92:93] op_sel:[1,0,0]
	v_pk_fma_f32 v[152:153], v[148:149], v[90:91], v[152:153] op_sel_hi:[0,1,1]
	v_pk_mul_f32 v[154:155], v[132:133], v[80:81] op_sel_hi:[0,1]
	v_pk_fma_f32 v[154:155], v[132:133], v[92:93], v[154:155] op_sel:[1,0,0]
	v_pk_fma_f32 v[154:155], v[134:135], v[152:153], v[154:155] op_sel_hi:[0,1,1]
	v_pk_fma_f32 v[154:155], v[148:149], v[100:101], v[154:155] op_sel:[1,0,0] neg_lo:[0,0,1] neg_hi:[0,0,1]
	v_cmp_eq_u32_e64 s[10:11], 6, v151
	v_cmp_eq_u32_e64 s[14:15], 7, v151
	v_pk_add_f32 v[88:89], v[62:63], v[80:81]
	v_pk_add_f32 v[90:91], v[64:65], v[88:89]
	v_pk_add_f32 v[62:63], v[66:67], v[92:93]
	v_pk_add_f32 v[64:65], v[98:99], v[62:63]
	v_pk_add_f32 v[66:67], v[86:87], v[152:153]
	v_pk_add_f32 v[94:95], v[102:103], v[66:67]
	v_pk_add_f32 v[86:87], v[96:97], v[154:155]
	v_pk_add_f32 v[98:99], v[116:117], v[86:87]
	v_pk_fma_f32 v[96:97], v[108:109], v[90:91], v[98:99] op_sel_hi:[0,1,1]
	v_pk_fma_f32 v[100:101], v[112:113], v[90:91], v[98:99] op_sel_hi:[0,1,1]
	v_pk_fma_f32 v[96:97], v[108:109], v[64:65], v[96:97] op_sel:[1,0,0]
	v_pk_fma_f32 v[100:101], v[112:113], v[64:65], v[100:101] op_sel:[1,0,0]
	v_pk_fma_f32 v[96:97], v[110:111], v[94:95], v[96:97] op_sel_hi:[0,1,1]
	v_pk_fma_f32 v[100:101], v[114:115], v[94:95], v[100:101] op_sel_hi:[0,1,1]
	v_pk_fma_f32 v[98:99], v[32:33], v[90:91], v[98:99] op_sel_hi:[0,1,1]
	v_pk_fma_f32 v[98:99], v[32:33], v[64:65], v[98:99] op_sel:[1,0,0]
	v_pk_fma_f32 v[98:99], v[34:35], v[94:95], v[98:99] op_sel_hi:[0,1,1]
	v_cndmask_b32_e64 v102, 0, v18, s[10:11]
	v_cndmask_b32_e64 v103, 0, v18, s[14:15]
	v_add_f32_dpp v98, v96, v98 wave_shl:1 row_mask:0xf bank_mask:0xf bound_ctrl:1
	v_add_f32_dpp v99, v97, v99 wave_shl:1 row_mask:0xf bank_mask:0xf bound_ctrl:1
	s_add_i32 s4, s34, 0
	s_cmpk_lt_i32 s4, 0x201
	s_cselect_b64 s[12:13], s[0:1], 0
	v_add_f32_dpp v98, v100, v98 wave_shr:1 row_mask:0xf bank_mask:0xf bound_ctrl:1
	v_add_f32_dpp v99, v101, v99 wave_shr:1 row_mask:0xf bank_mask:0xf bound_ctrl:1
	v_pk_fma_f32 v[98:99], v[20:21], v[150:151], v[98:99] op_sel_hi:[1,0,1] neg_lo:[0,0,1] neg_hi:[0,0,1]
	v_pk_add_f32 v[98:99], v[98:99], v[102:103] neg_lo:[0,1] neg_hi:[0,1]
	v_pk_mul_f32 v[116:117], v[98:99], v[98:99]
	v_add_f32_e32 v116, v116, v117
	v_cndmask_b32_e64 v117, 0, v116, s[12:13]
	v_add_f32_e32 v1, v1, v117
	s_add_i32 s5, s34, 5
	s_min_i32 s5, s5, 0x200
	s_mul_i32 s6, s5, 0x804
	s_add_i32 s6, s6, s35
	s_add_i32 s7, s6, 0x505014
	s_add_i32 s8, s6, 0x606018
	s_mul_i32 s9, s5, 0x180c
	s_add_i32 s9, s9, s33
	s_add_i32 s4, s34, 6
	s_min_i32 s4, s4, 0x200
	s_mul_i32 s4, s4, 0x804
	s_add_i32 s4, s4, s38
	buffer_load_dword v16, v28, s[20:23], s4 offen nt
	buffer_load_dwordx3 v[32:34], v27, s[24:27], s9 offen nt
	buffer_load_dword v20, v28, s[16:19], s7 offen nt
	buffer_load_dword v21, v28, s[16:19], s8 offen nt
	s_waitcnt vmcnt(8)
	v_mov_b32_dpp v96, v8 wave_shr:1 row_mask:0xf bank_mask:0xf bound_ctrl:1
	v_mov_b32_dpp v97, v9 wave_shr:1 row_mask:0xf bank_mask:0xf bound_ctrl:1
	v_mov_b32_dpp v98, v10 wave_shr:1 row_mask:0xf bank_mask:0xf bound_ctrl:1
	v_mov_b32_dpp v100, v8 wave_shl:1 row_mask:0xf bank_mask:0xf bound_ctrl:1
	v_mov_b32_dpp v101, v9 wave_shl:1 row_mask:0xf bank_mask:0xf bound_ctrl:1
	v_mov_b32_dpp v102, v10 wave_shl:1 row_mask:0xf bank_mask:0xf bound_ctrl:1
	s_add_i32 s4, s34, 4
	s_cmpk_lt_u32 s4, 0x201
	s_cselect_b64 s[12:13], s[40:41], 0
	v_cmp_eq_u32_e64 s[14:15], s37, v2
	s_and_b64 s[14:15], s[14:15], s[12:13]
	v_cndmask_b32_e64 v25, 0, 1, s[14:15]
	v_mul_f32_e64 v64, v8, v8
	v_mul_f32_e64 v65, v8, v9
	v_mul_f32_e64 v90, v8, v10
	v_mul_f32_e64 v91, v9, v9
	v_mul_f32_e64 v94, v9, v10
	v_mul_f32_e64 v95, v10, v10
	v_or_b32_dpp v29, v25, v25 wave_shr:1 row_mask:0xf bank_mask:0xf bound_ctrl:1
	s_nop 1
	v_or_b32_dpp v29, v25, v29 wave_shl:1 row_mask:0xf bank_mask:0xf bound_ctrl:1
	s_nop 1
	v_or_b32_dpp v52, v29, v29 wave_shr:1 row_mask:0xf bank_mask:0xf bound_ctrl:1
	s_nop 1
	v_or_b32_dpp v52, v29, v52 wave_shl:1 row_mask:0xf bank_mask:0xf bound_ctrl:1
	v_or3_b32 v25, v52, v30, v53
	v_or3_b32 v25, v25, v84, v85
	s_add_i32 s4, s34, 1
	s_cmpk_lt_u32 s4, 0x1ff
	s_cselect_b64 s[12:13], s[42:43], 0
	v_cmp_ne_u32_e64 s[30:31], 0, v25
	s_and_b64 s[30:31], s[30:31], s[12:13]
	v_cndmask_b32_e64 v25, 0, 1.0, s[30:31]
	v_add_f32_e64 v108, v8, v96
	v_add_f32_e64 v109, v9, v97
	v_add_f32_e64 v110, v10, v98
	v_fma_f32 v64, v96, v96, v64
	v_fma_f32 v65, v96, v97, v65
	v_fma_f32 v90, v96, v98, v90
	v_fma_f32 v91, v97, v97, v91
	v_fma_f32 v94, v97, v98, v94
	v_fma_f32 v95, v98, v98, v95
	v_add_f32_dpp v117, v25, v25 wave_shr:1 row_mask:0xf bank_mask:0xf bound_ctrl:1
	v_add_f32_e64 v108, v108, v100
	v_add_f32_e64 v109, v109, v101
	v_add_f32_e64 v110, v110, v102
	v_fma_f32 v111, v100, v100, v64
	v_fma_f32 v112, v100, v101, v65
	v_fma_f32 v113, v100, v102, v90
	v_fma_f32 v114, v101, v101, v91
	v_fma_f32 v115, v101, v102, v94
	v_fma_f32 v116, v102, v102, v95
	v_add_f32_dpp v117, v25, v117 wave_shl:1 row_mask:0xf bank_mask:0xf bound_ctrl:1
	v_pk_add_f32 v[64:65], v[44:45], v[108:109]
	v_pk_add_f32 v[44:45], v[54:55], v[110:111]
	v_pk_add_f32 v[54:55], v[118:119], v[112:113]
	v_pk_add_f32 v[90:91], v[122:123], v[114:115]
	v_pk_add_f32 v[94:95], v[124:125], v[116:117]
	v_mul_f32_e64 v132, v64, v22
	v_mul_f32_e64 v133, v65, v22
	v_mul_f32_e64 v134, v44, v22
	v_fma_f32 v25, v45, v22, v26
	v_mul_f32_e64 v29, v54, v22
	v_mul_f32_e64 v118, v55, v22
	v_fma_f32 v119, v90, v22, v26
	v_mul_f32_e64 v122, v91, v22
	v_fma_f32 v123, v94, v22, v26
	v_fma_f32 v25, -v132, v132, v25
	v_fma_f32 v29, -v132, v133, v29
	v_fma_f32 v118, -v132, v134, v118
	v_fma_f32 v119, -v133, v133, v119
	v_fma_f32 v122, -v133, v134, v122
	v_fma_f32 v123, -v134, v134, v123
	v_mul_f32_e64 v124, v122, v122
	v_mul_f32_e64 v125, v29, v123
	v_mul_f32_e64 v156, v118, v119
	v_mul_f32_e64 v157, v118, v118
	v_mul_f32_e64 v158, v25, v122
	v_mul_f32_e64 v159, v29, v29
	v_fma_f32 v124, v119, v123, -v124
	v_fma_f32 v125, v118, v122, -v125
	v_fma_f32 v156, v29, v122, -v156
	v_fma_f32 v157, v25, v123, -v157
	v_fma_f32 v158, v29, v118, -v158
	v_fma_f32 v159, v25, v119, -v159
	v_mul_f32_e64 v160, v25, v124
	v_fma_f32 v160, v29, v125, v160
	v_fma_f32 v160, v118, v156, v160
	v_rcp_f32_e32 v160, v160
	v_cmp_ne_u32_e64 vcc, s37, v31
	v_mul_f32_e64 v160, v160, v22
	v_cndmask_b32_e64 v160, 0, v160, s[30:31]
	v_cndmask_b32_e64 v25, 0, v18, vcc
	v_cndmask_b32_e64 v149, 0, v22, s[30:31]
	v_mul_f32_e64 v135, v124, v160
	v_mul_f32_e64 v144, v125, v160
	v_mul_f32_e64 v145, v156, v160
	v_mul_f32_e64 v146, v157, v160
	v_mul_f32_e64 v147, v158, v160
	v_mul_f32_e64 v148, v159, v160
	v_add_f32_e64 v150, v95, v25
	v_mov_b32_e32 v151, v31
	ds_write_b128 v23, v[132:135] offset:3072
	ds_write_b128 v23, v[144:147] offset:4096
	ds_write_b128 v23, v[148:151] offset:5120
	s_waitcnt lgkmcnt(0)
	s_barrier
	v_mov_b32_dpp v44, v4 wave_shr:1 row_mask:0xf bank_mask:0xf bound_ctrl:1
	v_mov_b32_dpp v45, v5 wave_shr:1 row_mask:0xf bank_mask:0xf bound_ctrl:1
	v_mov_b32_dpp v54, v4 wave_shl:1 row_mask:0xf bank_mask:0xf bound_ctrl:1
	v_mov_b32_dpp v55, v5 wave_shl:1 row_mask:0xf bank_mask:0xf bound_ctrl:1
	v_pk_mul_f32 v[64:65], v[4:5], v[8:9] op_sel_hi:[1,0]
	v_pk_mul_f32 v[90:91], v[4:5], v[8:9] op_sel:[0,1]
	v_pk_mul_f32 v[94:95], v[4:5], v[10:11] op_sel_hi:[1,0]
	v_pk_add_f32 v[118:119], v[4:5], v[44:45]
	v_pk_fma_f32 v[64:65], v[44:45], v[96:97], v[64:65] op_sel_hi:[1,0,1]
	v_pk_fma_f32 v[90:91], v[44:45], v[96:97], v[90:91] op_sel:[0,1,0]
	v_pk_fma_f32 v[94:95], v[44:45], v[98:99], v[94:95] op_sel_hi:[1,0,1]
	v_pk_add_f32 v[118:119], v[118:119], v[54:55]
	v_pk_fma_f32 v[64:65], v[54:55], v[100:101], v[64:65] op_sel_hi:[1,0,1]
	v_pk_fma_f32 v[90:91], v[54:55], v[100:101], v[90:91] op_sel:[0,1,0]
	v_pk_fma_f32 v[94:95], v[54:55], v[102:103], v[94:95] op_sel_hi:[1,0,1]
	v_pk_add_f32 v[44:45], v[50:51], v[118:119]
	v_pk_add_f32 v[50:51], v[82:83], v[64:65]
	v_pk_add_f32 v[54:55], v[56:57], v[90:91]
	v_pk_add_f32 v[56:57], v[58:59], v[94:95]
	v_pk_fma_f32 v[50:51], v[132:133], v[44:45], v[50:51] op_sel_hi:[0,1,1] neg_lo:[1,0,0] neg_hi:[1,0,0]
	v_pk_fma_f32 v[54:55], v[132:133], v[44:45], v[54:55] op_sel:[1,0,0] neg_lo:[1,0,0] neg_hi:[1,0,0]
	v_pk_fma_f32 v[56:57], v[134:135], v[44:45], v[56:57] op_sel_hi:[0,1,1] neg_lo:[1,0,0] neg_hi:[1,0,0]
	v_pk_mul_f32 v[58:59], v[134:135], v[50:51] op_sel:[1,0]
	v_pk_mul_f32 v[82:83], v[144:145], v[50:51] op_sel_hi:[0,1]
	v_pk_mul_f32 v[122:123], v[144:145], v[50:51] op_sel:[1,0]
	v_pk_fma_f32 v[58:59], v[144:145], v[54:55], v[58:59] op_sel_hi:[0,1,1]
	v_pk_fma_f32 v[82:83], v[146:147], v[54:55], v[82:83] op_sel_hi:[0,1,1]
	v_pk_fma_f32 v[122:123], v[146:147], v[54:55], v[122:123] op_sel:[1,0,0]
	v_pk_fma_f32 v[58:59], v[144:145], v[56:57], v[58:59] op_sel:[1,0,0]
	v_pk_fma_f32 v[82:83], v[146:147], v[56:57], v[82:83] op_sel:[1,0,0]
	v_pk_fma_f32 v[122:123], v[148:149], v[56:57], v[122:123] op_sel_hi:[0,1,1]
	v_pk_mul_f32 v[124:125], v[132:133], v[58:59] op_sel_hi:[0,1]
	v_pk_fma_f32 v[124:125], v[132:133], v[82:83], v[124:125] op_sel:[1,0,0]
	v_pk_fma_f32 v[124:125], v[134:135], v[122:123], v[124:125] op_sel_hi:[0,1,1]
	v_pk_fma_f32 v[124:125], v[148:149], v[44:45], v[124:125] op_sel:[1,0,0] neg_lo:[0,0,1] neg_hi:[0,0,1]
	v_cmp_eq_u32_e64 s[10:11], 6, v151
	v_cmp_eq_u32_e64 s[14:15], 7, v151
	v_pk_add_f32 v[44:45], v[88:89], v[58:59]
	v_pk_add_f32 v[50:51], v[62:63], v[82:83]
	v_pk_add_f32 v[54:55], v[66:67], v[122:123]
	v_pk_add_f32 v[56:57], v[86:87], v[124:125]
	v_pk_fma_f32 v[62:63], v[36:37], v[44:45], v[56:57] op_sel_hi:[0,1,1]
	v_pk_fma_f32 v[66:67], v[40:41], v[44:45], v[56:57] op_sel_hi:[0,1,1]
	v_pk_fma_f32 v[62:63], v[36:37], v[50:51], v[62:63] op_sel:[1,0,0]
	v_pk_fma_f32 v[66:67], v[40:41], v[50:51], v[66:67] op_sel:[1,0,0]
	v_pk_fma_f32 v[62:63], v[38:39], v[54:55], v[62:63] op_sel_hi:[0,1,1]
	v_pk_fma_f32 v[66:67], v[42:43], v[54:55], v[66:67] op_sel_hi:[0,1,1]
	v_pk_fma_f32 v[56:57], v[68:69], v[44:45], v[56:57] op_sel_hi:[0,1,1]
	v_pk_fma_f32 v[56:57], v[68:69], v[50:51], v[56:57] op_sel:[1,0,0]
	v_pk_fma_f32 v[56:57], v[70:71], v[54:55], v[56:57] op_sel_hi:[0,1,1]
	v_cndmask_b32_e64 v86, 0, v18, s[10:11]
	v_cndmask_b32_e64 v87, 0, v18, s[14:15]
	v_add_f32_dpp v56, v62, v56 wave_shl:1 row_mask:0xf bank_mask:0xf bound_ctrl:1
	v_add_f32_dpp v57, v63, v57 wave_shl:1 row_mask:0xf bank_mask:0xf bound_ctrl:1
	s_add_i32 s4, s34, 1
	s_cmpk_lt_i32 s4, 0x201
	s_cselect_b64 s[12:13], s[0:1], 0
	v_add_f32_dpp v56, v66, v56 wave_shr:1 row_mask:0xf bank_mask:0xf bound_ctrl:1
	v_add_f32_dpp v57, v67, v57 wave_shr:1 row_mask:0xf bank_mask:0xf bound_ctrl:1
	v_pk_fma_f32 v[56:57], v[46:47], v[150:151], v[56:57] op_sel_hi:[1,0,1] neg_lo:[0,0,1] neg_hi:[0,0,1]
	v_pk_add_f32 v[56:57], v[56:57], v[86:87] neg_lo:[0,1] neg_hi:[0,1]
	v_pk_mul_f32 v[88:89], v[56:57], v[56:57]
	v_add_f32_e32 v88, v88, v89
	v_cndmask_b32_e64 v89, 0, v88, s[12:13]
	v_add_f32_e32 v1, v1, v89
	s_add_i32 s5, s34, 6
	s_min_i32 s5, s5, 0x200
	s_mul_i32 s6, s5, 0x804
	s_add_i32 s6, s6, s35
	s_add_i32 s7, s6, 0x505014
	s_add_i32 s8, s6, 0x606018
	s_mul_i32 s9, s5, 0x180c
	s_add_i32 s9, s9, s33
	s_add_i32 s4, s34, 7
	s_min_i32 s4, s4, 0x200
	s_mul_i32 s4, s4, 0x804
	s_add_i32 s4, s4, s38
	buffer_load_dword v25, v28, s[20:23], s4 offen nt
	buffer_load_dwordx3 v[40:42], v27, s[24:27], s9 offen nt
	buffer_load_dword v36, v28, s[16:19], s7 offen nt
	buffer_load_dword v37, v28, s[16:19], s8 offen nt
	s_waitcnt vmcnt(8)
	v_mov_b32_dpp v44, v12 wave_shr:1 row_mask:0xf bank_mask:0xf bound_ctrl:1
	v_mov_b32_dpp v45, v13 wave_shr:1 row_mask:0xf bank_mask:0xf bound_ctrl:1
	v_mov_b32_dpp v46, v14 wave_shr:1 row_mask:0xf bank_mask:0xf bound_ctrl:1
	v_mov_b32_dpp v68, v12 wave_shl:1 row_mask:0xf bank_mask:0xf bound_ctrl:1
	v_mov_b32_dpp v69, v13 wave_shl:1 row_mask:0xf bank_mask:0xf bound_ctrl:1
	v_mov_b32_dpp v70, v14 wave_shl:1 row_mask:0xf bank_mask:0xf bound_ctrl:1
	s_add_i32 s4, s34, 5
	s_cmpk_lt_u32 s4, 0x201
	s_cselect_b64 s[12:13], s[40:41], 0
	v_cmp_eq_u32_e64 s[14:15], s37, v3
	s_and_b64 s[14:15], s[14:15], s[12:13]
	v_cndmask_b32_e64 v29, 0, 1, s[14:15]
	v_mul_f32_e64 v38, v12, v12
	v_mul_f32_e64 v39, v12, v13
	v_mul_f32_e64 v50, v12, v14
	v_mul_f32_e64 v51, v13, v13
	v_mul_f32_e64 v54, v13, v14
	v_mul_f32_e64 v55, v14, v14
	v_or_b32_dpp v31, v29, v29 wave_shr:1 row_mask:0xf bank_mask:0xf bound_ctrl:1
	s_nop 1
	v_or_b32_dpp v31, v29, v31 wave_shl:1 row_mask:0xf bank_mask:0xf bound_ctrl:1
	s_nop 1
	v_or_b32_dpp v85, v31, v31 wave_shr:1 row_mask:0xf bank_mask:0xf bound_ctrl:1
	s_nop 1
	v_or_b32_dpp v85, v31, v85 wave_shl:1 row_mask:0xf bank_mask:0xf bound_ctrl:1
	v_or3_b32 v29, v85, v52, v30
	v_or3_b32 v29, v29, v53, v84
	s_add_i32 s4, s34, 2
	s_cmpk_lt_u32 s4, 0x1ff
	s_cselect_b64 s[12:13], s[42:43], 0
	v_cmp_ne_u32_e64 s[30:31], 0, v29
	s_and_b64 s[30:31], s[30:31], s[12:13]
	v_cndmask_b32_e64 v29, 0, 1.0, s[30:31]
	v_add_f32_e64 v56, v12, v44
	v_add_f32_e64 v57, v13, v45
	v_add_f32_e64 v62, v14, v46
	v_fma_f32 v38, v44, v44, v38
	v_fma_f32 v39, v44, v45, v39
	v_fma_f32 v50, v44, v46, v50
	v_fma_f32 v51, v45, v45, v51
	v_fma_f32 v54, v45, v46, v54
	v_fma_f32 v55, v46, v46, v55
	v_add_f32_dpp v89, v29, v29 wave_shr:1 row_mask:0xf bank_mask:0xf bound_ctrl:1
	v_add_f32_e64 v56, v56, v68
	v_add_f32_e64 v57, v57, v69
	v_add_f32_e64 v62, v62, v70
	v_fma_f32 v63, v68, v68, v38
	v_fma_f32 v66, v68, v69, v39
	v_fma_f32 v67, v68, v70, v50
	v_fma_f32 v86, v69, v69, v51
	v_fma_f32 v87, v69, v70, v54
	v_fma_f32 v88, v70, v70, v55
	v_add_f32_dpp v89, v29, v89 wave_shl:1 row_mask:0xf bank_mask:0xf bound_ctrl:1
	v_pk_add_f32 v[38:39], v[108:109], v[56:57]
	v_pk_add_f32 v[50:51], v[60:61], v[38:39]
	v_pk_add_f32 v[54:55], v[110:111], v[62:63]
	v_pk_add_f32 v[60:61], v[136:137], v[54:55]
	v_pk_add_f32 v[108:109], v[112:113], v[66:67]
	v_pk_add_f32 v[110:111], v[138:139], v[108:109]
	v_pk_add_f32 v[112:113], v[114:115], v[86:87]
	v_pk_add_f32 v[132:133], v[140:141], v[112:113]
	v_pk_add_f32 v[114:115], v[116:117], v[88:89]
	v_pk_add_f32 v[134:135], v[142:143], v[114:115]
	v_mul_f32_e64 v136, v50, v22
	v_mul_f32_e64 v137, v51, v22
	v_mul_f32_e64 v138, v60, v22
	v_fma_f32 v29, v61, v22, v26
	v_mul_f32_e64 v31, v110, v22
	v_mul_f32_e64 v116, v111, v22
	v_fma_f32 v117, v132, v22, v26
	v_mul_f32_e64 v148, v133, v22
	v_fma_f32 v149, v134, v22, v26
	v_fma_f32 v29, -v136, v136, v29
	v_fma_f32 v31, -v136, v137, v31
	v_fma_f32 v116, -v136, v138, v116
	v_fma_f32 v117, -v137, v137, v117
	v_fma_f32 v148, -v137, v138, v148
	v_fma_f32 v149, -v138, v138, v149
	v_mul_f32_e64 v150, v148, v148
	v_mul_f32_e64 v151, v31, v149
	v_mul_f32_e64 v156, v116, v117
	v_mul_f32_e64 v157, v116, v116
	v_mul_f32_e64 v158, v29, v148
	v_mul_f32_e64 v159, v31, v31
	v_fma_f32 v150, v117, v149, -v150
	v_fma_f32 v151, v116, v148, -v151
	v_fma_f32 v156, v31, v148, -v156
	v_fma_f32 v157, v29, v149, -v157
	v_fma_f32 v158, v31, v116, -v158
	v_fma_f32 v159, v29, v117, -v159
	v_mul_f32_e64 v160, v29, v150
	v_fma_f32 v160, v31, v151, v160
	v_fma_f32 v160, v116, v156, v160
	v_rcp_f32_e32 v160, v160
	v_cmp_ne_u32_e64 vcc, s37, v24
	v_mul_f32_e64 v160, v160, v22
	v_cndmask_b32_e64 v160, 0, v160, s[30:31]
	v_cndmask_b32_e64 v29, 0, v18, vcc
	v_cndmask_b32_e64 v145, 0, v22, s[30:31]
	v_mul_f32_e64 v139, v150, v160
	v_mul_f32_e64 v140, v151, v160
	v_mul_f32_e64 v141, v156, v160
	v_mul_f32_e64 v142, v157, v160
	v_mul_f32_e64 v143, v158, v160
	v_mul_f32_e64 v144, v159, v160
	v_add_f32_e64 v146, v135, v29
	v_mov_b32_e32 v147, v24
	ds_write_b128 v23, v[136:139]
	ds_write_b128 v23, v[140:143] offset:1024
	ds_write_b128 v23, v[144:147] offset:2048
	s_waitcnt lgkmcnt(0)
	s_barrier
	v_mov_b32_dpp v50, v6 wave_shr:1 row_mask:0xf bank_mask:0xf bound_ctrl:1
	v_mov_b32_dpp v51, v7 wave_shr:1 row_mask:0xf bank_mask:0xf bound_ctrl:1
	v_mov_b32_dpp v60, v6 wave_shl:1 row_mask:0xf bank_mask:0xf bound_ctrl:1
	v_mov_b32_dpp v61, v7 wave_shl:1 row_mask:0xf bank_mask:0xf bound_ctrl:1
	v_pk_mul_f32 v[110:111], v[6:7], v[12:13] op_sel_hi:[1,0]
	v_pk_mul_f32 v[116:117], v[6:7], v[12:13] op_sel:[0,1]
	v_pk_mul_f32 v[132:133], v[6:7], v[14:15] op_sel_hi:[1,0]
	v_pk_add_f32 v[134:135], v[6:7], v[50:51]
	v_pk_fma_f32 v[110:111], v[50:51], v[44:45], v[110:111] op_sel_hi:[1,0,1]
	v_pk_fma_f32 v[116:117], v[50:51], v[44:45], v[116:117] op_sel:[0,1,0]
	v_pk_fma_f32 v[132:133], v[50:51], v[46:47], v[132:133] op_sel_hi:[1,0,1]
	v_pk_add_f32 v[134:135], v[134:135], v[60:61]
	v_pk_fma_f32 v[110:111], v[60:61], v[68:69], v[110:111] op_sel_hi:[1,0,1]
	v_pk_fma_f32 v[116:117], v[60:61], v[68:69], v[116:117] op_sel:[0,1,0]
	v_pk_fma_f32 v[132:133], v[60:61], v[70:71], v[132:133] op_sel_hi:[1,0,1]
	v_pk_add_f32 v[50:51], v[118:119], v[134:135]
	v_pk_add_f32 v[60:61], v[130:131], v[50:51]
	v_pk_add_f32 v[118:119], v[64:65], v[110:111]
	v_pk_add_f32 v[130:131], v[120:121], v[118:119]
	v_pk_add_f32 v[64:65], v[90:91], v[116:117]
	v_pk_add_f32 v[120:121], v[126:127], v[64:65]
	v_pk_add_f32 v[90:91], v[94:95], v[132:133]
	v_pk_add_f32 v[126:127], v[128:129], v[90:91]
	v_pk_fma_f32 v[130:131], v[136:137], v[60:61], v[130:131] op_sel_hi:[0,1,1] neg_lo:[1,0,0] neg_hi:[1,0,0]
	v_pk_fma_f32 v[120:121], v[136:137], v[60:61], v[120:121] op_sel:[1,0,0] neg_lo:[1,0,0] neg_hi:[1,0,0]
	v_pk_fma_f32 v[126:127], v[138:139], v[60:61], v[126:127] op_sel_hi:[0,1,1] neg_lo:[1,0,0] neg_hi:[1,0,0]
	v_pk_mul_f32 v[94:95], v[138:139], v[130:131] op_sel:[1,0]
	v_pk_mul_f32 v[128:129], v[140:141], v[130:131] op_sel_hi:[0,1]
	v_pk_mul_f32 v[148:149], v[140:141], v[130:131] op_sel:[1,0]
	v_pk_fma_f32 v[94:95], v[140:141], v[120:121], v[94:95] op_sel_hi:[0,1,1]
	v_pk_fma_f32 v[128:129], v[142:143], v[120:121], v[128:129] op_sel_hi:[0,1,1]
	v_pk_fma_f32 v[148:149], v[142:143], v[120:121], v[148:149] op_sel:[1,0,0]
	v_pk_fma_f32 v[94:95], v[140:141], v[126:127], v[94:95] op_sel:[1,0,0]
	v_pk_fma_f32 v[128:129], v[142:143], v[126:127], v[128:129] op_sel:[1,0,0]
	v_pk_fma_f32 v[148:149], v[144:145], v[126:127], v[148:149] op_sel_hi:[0,1,1]
	v_pk_mul_f32 v[150:151], v[136:137], v[94:95] op_sel_hi:[0,1]
	v_pk_fma_f32 v[150:151], v[136:137], v[128:129], v[150:151] op_sel:[1,0,0]
	v_pk_fma_f32 v[150:151], v[138:139], v[148:149], v[150:151] op_sel_hi:[0,1,1]
	v_pk_fma_f32 v[150:151], v[144:145], v[60:61], v[150:151] op_sel:[1,0,0] neg_lo:[0,0,1] neg_hi:[0,0,1]
	v_cmp_eq_u32_e64 s[10:11], 6, v147
	v_cmp_eq_u32_e64 s[14:15], 7, v147
	v_pk_add_f32 v[60:61], v[58:59], v[94:95]
	v_pk_add_f32 v[120:121], v[80:81], v[60:61]
	v_pk_add_f32 v[58:59], v[82:83], v[128:129]
	v_pk_add_f32 v[80:81], v[92:93], v[58:59]
	v_pk_add_f32 v[82:83], v[122:123], v[148:149]
	v_pk_add_f32 v[92:93], v[152:153], v[82:83]
	v_pk_add_f32 v[122:123], v[124:125], v[150:151]
	v_pk_add_f32 v[126:127], v[154:155], v[122:123]
	v_pk_fma_f32 v[124:125], v[72:73], v[120:121], v[126:127] op_sel_hi:[0,1,1]
	v_pk_fma_f32 v[130:131], v[76:77], v[120:121], v[126:127] op_sel_hi:[0,1,1]
	v_pk_fma_f32 v[124:125], v[72:73], v[80:81], v[124:125] op_sel:[1,0,0]
	v_pk_fma_f32 v[130:131], v[76:77], v[80:81], v[130:131] op_sel:[1,0,0]
	v_pk_fma_f32 v[124:125], v[74:75], v[92:93], v[124:125] op_sel_hi:[0,1,1]
	v_pk_fma_f32 v[130:131], v[78:79], v[92:93], v[130:131] op_sel_hi:[0,1,1]
	v_pk_fma_f32 v[126:127], v[104:105], v[120:121], v[126:127] op_sel_hi:[0,1,1]
	v_pk_fma_f32 v[126:127], v[104:105], v[80:81], v[126:127] op_sel:[1,0,0]
	v_pk_fma_f32 v[126:127], v[106:107], v[92:93], v[126:127] op_sel_hi:[0,1,1]
	v_cndmask_b32_e64 v152, 0, v18, s[10:11]
	v_cndmask_b32_e64 v153, 0, v18, s[14:15]
	v_add_f32_dpp v126, v124, v126 wave_shl:1 row_mask:0xf bank_mask:0xf bound_ctrl:1
	v_add_f32_dpp v127, v125, v127 wave_shl:1 row_mask:0xf bank_mask:0xf bound_ctrl:1
	s_add_i32 s4, s34, 2
	s_cmpk_lt_i32 s4, 0x201
	s_cselect_b64 s[12:13], s[0:1], 0
	v_add_f32_dpp v126, v130, v126 wave_shr:1 row_mask:0xf bank_mask:0xf bound_ctrl:1
	v_add_f32_dpp v127, v131, v127 wave_shr:1 row_mask:0xf bank_mask:0xf bound_ctrl:1
	v_pk_fma_f32 v[126:127], v[48:49], v[146:147], v[126:127] op_sel_hi:[1,0,1] neg_lo:[0,0,1] neg_hi:[0,0,1]
	v_pk_add_f32 v[126:127], v[126:127], v[152:153] neg_lo:[0,1] neg_hi:[0,1]
	v_pk_mul_f32 v[154:155], v[126:127], v[126:127]
	v_add_f32_e32 v154, v154, v155
	v_cndmask_b32_e64 v155, 0, v154, s[12:13]
	v_add_f32_e32 v1, v1, v155
	s_add_i32 s5, s34, 7
	s_min_i32 s5, s5, 0x200
	s_mul_i32 s6, s5, 0x804
	s_add_i32 s6, s6, s35
	s_add_i32 s7, s6, 0x505014
	s_add_i32 s8, s6, 0x606018
	s_mul_i32 s9, s5, 0x180c
	s_add_i32 s9, s9, s33
	s_add_i32 s4, s34, 8
	s_min_i32 s4, s4, 0x200
	s_mul_i32 s4, s4, 0x804
	s_add_i32 s4, s4, s38
	buffer_load_dword v24, v28, s[20:23], s4 offen nt
	buffer_load_dwordx3 v[72:74], v27, s[24:27], s9 offen nt
	buffer_load_dword v48, v28, s[16:19], s7 offen nt
	buffer_load_dword v49, v28, s[16:19], s8 offen nt
	s_waitcnt vmcnt(8)
	v_mov_b32_dpp v76, v32 wave_shr:1 row_mask:0xf bank_mask:0xf bound_ctrl:1
	v_mov_b32_dpp v77, v33 wave_shr:1 row_mask:0xf bank_mask:0xf bound_ctrl:1
	v_mov_b32_dpp v78, v34 wave_shr:1 row_mask:0xf bank_mask:0xf bound_ctrl:1
	v_mov_b32_dpp v104, v32 wave_shl:1 row_mask:0xf bank_mask:0xf bound_ctrl:1
	v_mov_b32_dpp v105, v33 wave_shl:1 row_mask:0xf bank_mask:0xf bound_ctrl:1
	v_mov_b32_dpp v106, v34 wave_shl:1 row_mask:0xf bank_mask:0xf bound_ctrl:1
	s_add_i32 s4, s34, 6
	s_cmpk_lt_u32 s4, 0x201
	s_cselect_b64 s[12:13], s[40:41], 0
	v_cmp_eq_u32_e64 s[14:15], s37, v16
	s_and_b64 s[14:15], s[14:15], s[12:13]
	v_cndmask_b32_e64 v29, 0, 1, s[14:15]
	v_mul_f32_e64 v80, v32, v32
	v_mul_f32_e64 v81, v32, v33
	v_mul_f32_e64 v92, v32, v34
	v_mul_f32_e64 v93, v33, v33
	v_mul_f32_e64 v120, v33, v34
	v_mul_f32_e64 v121, v34, v34
	v_or_b32_dpp v31, v29, v29 wave_shr:1 row_mask:0xf bank_mask:0xf bound_ctrl:1
	s_nop 1
	v_or_b32_dpp v31, v29, v31 wave_shl:1 row_mask:0xf bank_mask:0xf bound_ctrl:1
	s_nop 1
	v_or_b32_dpp v84, v31, v31 wave_shr:1 row_mask:0xf bank_mask:0xf bound_ctrl:1
	s_nop 1
	v_or_b32_dpp v84, v31, v84 wave_shl:1 row_mask:0xf bank_mask:0xf bound_ctrl:1
	v_or3_b32 v29, v84, v85, v52
	v_or3_b32 v29, v29, v30, v53
	s_add_i32 s4, s34, 3
	s_cmpk_lt_u32 s4, 0x1ff
	s_cselect_b64 s[12:13], s[42:43], 0
	v_cmp_ne_u32_e64 s[30:31], 0, v29
	s_and_b64 s[30:31], s[30:31], s[12:13]
	v_cndmask_b32_e64 v29, 0, 1.0, s[30:31]
	v_add_f32_e64 v124, v32, v76
	v_add_f32_e64 v125, v33, v77
	v_add_f32_e64 v126, v34, v78
	v_fma_f32 v80, v76, v76, v80
	v_fma_f32 v81, v76, v77, v81
	v_fma_f32 v92, v76, v78, v92
	v_fma_f32 v93, v77, v77, v93
	v_fma_f32 v120, v77, v78, v120
	v_fma_f32 v121, v78, v78, v121
	v_add_f32_dpp v139, v29, v29 wave_shr:1 row_mask:0xf bank_mask:0xf bound_ctrl:1
	v_add_f32_e64 v124, v124, v104
	v_add_f32_e64 v125, v125, v105
	v_add_f32_e64 v126, v126, v106
	v_fma_f32 v127, v104, v104, v80
	v_fma_f32 v130, v104, v105, v81
	v_fma_f32 v131, v104, v106, v92
	v_fma_f32 v136, v105, v105, v93
	v_fma_f32 v137, v105, v106, v120
	v_fma_f32 v138, v106, v106, v121
	v_add_f32_dpp v139, v29, v139 wave_shl:1 row_mask:0xf bank_mask:0xf bound_ctrl:1
	v_pk_add_f32 v[80:81], v[38:39], v[124:125]
	v_pk_add_f32 v[38:39], v[54:55], v[126:127]
	v_pk_add_f32 v[54:55], v[108:109], v[130:131]
	v_pk_add_f32 v[92:93], v[112:113], v[136:137]
	v_pk_add_f32 v[108:109], v[114:115], v[138:139]
	v_mul_f32_e64 v112, v80, v22
	v_mul_f32_e64 v113, v81, v22
	v_mul_f32_e64 v114, v38, v22
	v_fma_f32 v29, v39, v22, v26
	v_mul_f32_e64 v31, v54, v22
	v_mul_f32_e64 v120, v55, v22
	v_fma_f32 v121, v92, v22, v26
	v_mul_f32_e64 v152, v93, v22
	v_fma_f32 v153, v108, v22, v26
	v_fma_f32 v29, -v112, v112, v29
	v_fma_f32 v31, -v112, v113, v31
	v_fma_f32 v120, -v112, v114, v120
	v_fma_f32 v121, -v113, v113, v121
	v_fma_f32 v152, -v113, v114, v152
	v_fma_f32 v153, -v114, v114, v153
	v_mul_f32_e64 v154, v152, v152
	v_mul_f32_e64 v155, v31, v153
	v_mul_f32_e64 v156, v120, v121
	v_mul_f32_e64 v157, v120, v120
	v_mul_f32_e64 v158, v29, v152
	v_mul_f32_e64 v159, v31, v31
	v_fma_f32 v154, v121, v153, -v154
	v_fma_f32 v155, v120, v152, -v155
	v_fma_f32 v156, v31, v152, -v156
	v_fma_f32 v157, v29, v153, -v157
	v_fma_f32 v158, v31, v120, -v158
	v_fma_f32 v159, v29, v121, -v159
	v_mul_f32_e64 v160, v29, v154
	v_fma_f32 v160, v31, v155, v160
	v_fma_f32 v160, v120, v156, v160
	v_rcp_f32_e32 v160, v160
	v_cmp_ne_u32_e64 vcc, s37, v17
	v_mul_f32_e64 v160, v160, v22
	v_cndmask_b32_e64 v160, 0, v160, s[30:31]
	v_cndmask_b32_e64 v29, 0, v18, vcc
	v_cndmask_b32_e64 v145, 0, v22, s[30:31]
	v_mul_f32_e64 v115, v154, v160
	v_mul_f32_e64 v140, v155, v160
	v_mul_f32_e64 v141, v156, v160
	v_mul_f32_e64 v142, v157, v160
	v_mul_f32_e64 v143, v158, v160
	v_mul_f32_e64 v144, v159, v160
	v_add_f32_e64 v146, v109, v29
	v_mov_b32_e32 v147, v17
	ds_write_b128 v23, v[112:115] offset:3072
	ds_write_b128 v23, v[140:143] offset:4096
	ds_write_b128 v23, v[144:147] offset:5120
	s_waitcnt lgkmcnt(0)
	s_barrier
	v_mov_b32_dpp v38, v20 wave_shr:1 row_mask:0xf bank_mask:0xf bound_ctrl:1
	v_mov_b32_dpp v39, v21 wave_shr:1 row_mask:0xf bank_mask:0xf bound_ctrl:1
	v_mov_b32_dpp v54, v20 wave_shl:1 row_mask:0xf bank_mask:0xf bound_ctrl:1
	v_mov_b32_dpp v55, v21 wave_shl:1 row_mask:0xf bank_mask:0xf bound_ctrl:1
	v_pk_mul_f32 v[80:81], v[20:21], v[32:33] op_sel_hi:[1,0]
	v_pk_mul_f32 v[92:93], v[20:21], v[32:33] op_sel:[0,1]
	v_pk_mul_f32 v[108:109], v[20:21], v[34:35] op_sel_hi:[1,0]
	v_pk_add_f32 v[120:121], v[20:21], v[38:39]
	v_pk_fma_f32 v[80:81], v[38:39], v[76:77], v[80:81] op_sel_hi:[1,0,1]
	v_pk_fma_f32 v[92:93], v[38:39], v[76:77], v[92:93] op_sel:[0,1,0]
	v_pk_fma_f32 v[108:109], v[38:39], v[78:79], v[108:109] op_sel_hi:[1,0,1]
	v_pk_add_f32 v[120:121], v[120:121], v[54:55]
	v_pk_fma_f32 v[80:81], v[54:55], v[104:105], v[80:81] op_sel_hi:[1,0,1]
	v_pk_fma_f32 v[92:93], v[54:55], v[104:105], v[92:93] op_sel:[0,1,0]
	v_pk_fma_f32 v[108:109], v[54:55], v[106:107], v[108:109] op_sel_hi:[1,0,1]
	v_pk_add_f32 v[38:39], v[50:51], v[120:121]
	v_pk_add_f32 v[50:51], v[118:119], v[80:81]
	v_pk_add_f32 v[54:55], v[64:65], v[92:93]
	v_pk_add_f32 v[64:65], v[90:91], v[108:109]
	v_pk_fma_f32 v[50:51], v[112:113], v[38:39], v[50:51] op_sel_hi:[0,1,1] neg_lo:[1,0,0] neg_hi:[1,0,0]
	v_pk_fma_f32 v[54:55], v[112:113], v[38:39], v[54:55] op_sel:[1,0,0] neg_lo:[1,0,0] neg_hi:[1,0,0]
	v_pk_fma_f32 v[64:65], v[114:115], v[38:39], v[64:65] op_sel_hi:[0,1,1] neg_lo:[1,0,0] neg_hi:[1,0,0]
	v_pk_mul_f32 v[90:91], v[114:115], v[50:51] op_sel:[1,0]
	v_pk_mul_f32 v[118:119], v[140:141], v[50:51] op_sel_hi:[0,1]
	v_pk_mul_f32 v[152:153], v[140:141], v[50:51] op_sel:[1,0]
	v_pk_fma_f32 v[90:91], v[140:141], v[54:55], v[90:91] op_sel_hi:[0,1,1]
	v_pk_fma_f32 v[118:119], v[142:143], v[54:55], v[118:119] op_sel_hi:[0,1,1]
	v_pk_fma_f32 v[152:153], v[142:143], v[54:55], v[152:153] op_sel:[1,0,0]
	v_pk_fma_f32 v[90:91], v[140:141], v[64:65], v[90:91] op_sel:[1,0,0]
	v_pk_fma_f32 v[118:119], v[142:143], v[64:65], v[118:119] op_sel:[1,0,0]
	v_pk_fma_f32 v[152:153], v[144:145], v[64:65], v[152:153] op_sel_hi:[0,1,1]
	v_pk_mul_f32 v[154:155], v[112:113], v[90:91] op_sel_hi:[0,1]
	v_pk_fma_f32 v[154:155], v[112:113], v[118:119], v[154:155] op_sel:[1,0,0]
	v_pk_fma_f32 v[154:155], v[114:115], v[152:153], v[154:155] op_sel_hi:[0,1,1]
	v_pk_fma_f32 v[154:155], v[144:145], v[38:39], v[154:155] op_sel:[1,0,0] neg_lo:[0,0,1] neg_hi:[0,0,1]
	v_cmp_eq_u32_e64 s[10:11], 6, v147
	v_cmp_eq_u32_e64 s[14:15], 7, v147
	v_pk_add_f32 v[38:39], v[60:61], v[90:91]
	v_pk_add_f32 v[50:51], v[58:59], v[118:119]
	v_pk_add_f32 v[54:55], v[82:83], v[152:153]
	v_pk_add_f32 v[58:59], v[122:123], v[154:155]
	v_pk_fma_f32 v[60:61], v[96:97], v[38:39], v[58:59] op_sel_hi:[0,1,1]
	v_pk_fma_f32 v[64:65], v[100:101], v[38:39], v[58:59] op_sel_hi:[0,1,1]
	v_pk_fma_f32 v[60:61], v[96:97], v[50:51], v[60:61] op_sel:[1,0,0]
	v_pk_fma_f32 v[64:65], v[100:101], v[50:51], v[64:65] op_sel:[1,0,0]
	v_pk_fma_f32 v[60:61], v[98:99], v[54:55], v[60:61] op_sel_hi:[0,1,1]
	v_pk_fma_f32 v[64:65], v[102:103], v[54:55], v[64:65] op_sel_hi:[0,1,1]
	v_pk_fma_f32 v[58:59], v[8:9], v[38:39], v[58:59] op_sel_hi:[0,1,1]
	v_pk_fma_f32 v[58:59], v[8:9], v[50:51], v[58:59] op_sel:[1,0,0]
	v_pk_fma_f32 v[58:59], v[10:11], v[54:55], v[58:59] op_sel_hi:[0,1,1]
	v_cndmask_b32_e64 v82, 0, v18, s[10:11]
	v_cndmask_b32_e64 v83, 0, v18, s[14:15]
	v_add_f32_dpp v58, v60, v58 wave_shl:1 row_mask:0xf bank_mask:0xf bound_ctrl:1
	v_add_f32_dpp v59, v61, v59 wave_shl:1 row_mask:0xf bank_mask:0xf bound_ctrl:1
	s_add_i32 s4, s34, 3
	s_cmpk_lt_i32 s4, 0x201
	s_cselect_b64 s[12:13], s[0:1], 0
	v_add_f32_dpp v58, v64, v58 wave_shr:1 row_mask:0xf bank_mask:0xf bound_ctrl:1
	v_add_f32_dpp v59, v65, v59 wave_shr:1 row_mask:0xf bank_mask:0xf bound_ctrl:1
	v_pk_fma_f32 v[58:59], v[4:5], v[146:147], v[58:59] op_sel_hi:[1,0,1] neg_lo:[0,0,1] neg_hi:[0,0,1]
	v_pk_add_f32 v[58:59], v[58:59], v[82:83] neg_lo:[0,1] neg_hi:[0,1]
	v_pk_mul_f32 v[122:123], v[58:59], v[58:59]
	v_add_f32_e32 v122, v122, v123
	v_cndmask_b32_e64 v123, 0, v122, s[12:13]
	v_add_f32_e32 v1, v1, v123
	s_add_i32 s5, s34, 8
	s_min_i32 s5, s5, 0x200
	s_mul_i32 s6, s5, 0x804
	s_add_i32 s6, s6, s35
	s_add_i32 s7, s6, 0x505014
	s_add_i32 s8, s6, 0x606018
	s_mul_i32 s9, s5, 0x180c
	s_add_i32 s9, s9, s33
	s_add_i32 s4, s34, 9
	s_min_i32 s4, s4, 0x200
	s_mul_i32 s4, s4, 0x804
	s_add_i32 s4, s4, s38
	buffer_load_dword v17, v28, s[20:23], s4 offen nt
	buffer_load_dwordx3 v[8:10], v27, s[24:27], s9 offen nt
	buffer_load_dword v4, v28, s[16:19], s7 offen nt
	buffer_load_dword v5, v28, s[16:19], s8 offen nt
	s_waitcnt vmcnt(8)
	v_mov_b32_dpp v96, v40 wave_shr:1 row_mask:0xf bank_mask:0xf bound_ctrl:1
	v_mov_b32_dpp v97, v41 wave_shr:1 row_mask:0xf bank_mask:0xf bound_ctrl:1
	v_mov_b32_dpp v98, v42 wave_shr:1 row_mask:0xf bank_mask:0xf bound_ctrl:1
	v_mov_b32_dpp v100, v40 wave_shl:1 row_mask:0xf bank_mask:0xf bound_ctrl:1
	v_mov_b32_dpp v101, v41 wave_shl:1 row_mask:0xf bank_mask:0xf bound_ctrl:1
	v_mov_b32_dpp v102, v42 wave_shl:1 row_mask:0xf bank_mask:0xf bound_ctrl:1
	s_add_i32 s4, s34, 7
	s_cmpk_lt_u32 s4, 0x201
	s_cselect_b64 s[12:13], s[40:41], 0
	v_cmp_eq_u32_e64 s[14:15], s37, v25
	s_and_b64 s[14:15], s[14:15], s[12:13]
	v_cndmask_b32_e64 v29, 0, 1, s[14:15]
	v_mul_f32_e64 v38, v40, v40
	v_mul_f32_e64 v39, v40, v41
	v_mul_f32_e64 v50, v40, v42
	v_mul_f32_e64 v51, v41, v41
	v_mul_f32_e64 v54, v41, v42
	v_mul_f32_e64 v55, v42, v42
	v_or_b32_dpp v31, v29, v29 wave_shr:1 row_mask:0xf bank_mask:0xf bound_ctrl:1
	s_nop 1
	v_or_b32_dpp v31, v29, v31 wave_shl:1 row_mask:0xf bank_mask:0xf bound_ctrl:1
	s_nop 1
	v_or_b32_dpp v53, v31, v31 wave_shr:1 row_mask:0xf bank_mask:0xf bound_ctrl:1
	s_nop 1
	v_or_b32_dpp v53, v31, v53 wave_shl:1 row_mask:0xf bank_mask:0xf bound_ctrl:1
	v_or3_b32 v29, v53, v84, v85
	v_or3_b32 v29, v29, v52, v30
	s_add_i32 s4, s34, 4
	s_cmpk_lt_u32 s4, 0x1ff
	s_cselect_b64 s[12:13], s[42:43], 0
	v_cmp_ne_u32_e64 s[30:31], 0, v29
	s_and_b64 s[30:31], s[30:31], s[12:13]
	v_cndmask_b32_e64 v29, 0, 1.0, s[30:31]
	v_add_f32_e64 v58, v40, v96
	v_add_f32_e64 v59, v41, v97
	v_add_f32_e64 v60, v42, v98
	v_fma_f32 v38, v96, v96, v38
	v_fma_f32 v39, v96, v97, v39
	v_fma_f32 v50, v96, v98, v50
	v_fma_f32 v51, v97, v97, v51
	v_fma_f32 v54, v97, v98, v54
	v_fma_f32 v55, v98, v98, v55
	v_add_f32_dpp v113, v29, v29 wave_shr:1 row_mask:0xf bank_mask:0xf bound_ctrl:1
	v_add_f32_e64 v58, v58, v100
	v_add_f32_e64 v59, v59, v101
	v_add_f32_e64 v60, v60, v102
	v_fma_f32 v61, v100, v100, v38
	v_fma_f32 v64, v100, v101, v39
	v_fma_f32 v65, v100, v102, v50
	v_fma_f32 v82, v101, v101, v51
	v_fma_f32 v83, v101, v102, v54
	v_fma_f32 v112, v102, v102, v55
	v_add_f32_dpp v113, v29, v113 wave_shl:1 row_mask:0xf bank_mask:0xf bound_ctrl:1
	v_pk_add_f32 v[38:39], v[124:125], v[58:59]
	v_pk_add_f32 v[50:51], v[56:57], v[38:39]
	v_pk_add_f32 v[54:55], v[126:127], v[60:61]
	v_pk_add_f32 v[56:57], v[62:63], v[54:55]
	v_pk_add_f32 v[62:63], v[130:131], v[64:65]
	v_pk_add_f32 v[114:115], v[66:67], v[62:63]
	v_pk_add_f32 v[66:67], v[136:137], v[82:83]
	v_pk_add_f32 v[122:123], v[86:87], v[66:67]
	v_pk_add_f32 v[86:87], v[138:139], v[112:113]
	v_pk_add_f32 v[124:125], v[88:89], v[86:87]
	v_mul_f32_e64 v136, v50, v22
	v_mul_f32_e64 v137, v51, v22
	v_mul_f32_e64 v138, v56, v22
	v_fma_f32 v29, v57, v22, v26
	v_mul_f32_e64 v31, v114, v22
	v_mul_f32_e64 v88, v115, v22
	v_fma_f32 v89, v122, v22, v26
	v_mul_f32_e64 v126, v123, v22
	v_fma_f32 v127, v124, v22, v26
	v_fma_f32 v29, -v136, v136, v29
	v_fma_f32 v31, -v136, v137, v31
	v_fma_f32 v88, -v136, v138, v88
	v_fma_f32 v89, -v137, v137, v89
	v_fma_f32 v126, -v137, v138, v126
	v_fma_f32 v127, -v138, v138, v127
	v_mul_f32_e64 v130, v126, v126
	v_mul_f32_e64 v131, v31, v127
	v_mul_f32_e64 v156, v88, v89
	v_mul_f32_e64 v157, v88, v88
	v_mul_f32_e64 v158, v29, v126
	v_mul_f32_e64 v159, v31, v31
	v_fma_f32 v130, v89, v127, -v130
	v_fma_f32 v131, v88, v126, -v131
	v_fma_f32 v156, v31, v126, -v156
	v_fma_f32 v157, v29, v127, -v157
	v_fma_f32 v158, v31, v88, -v158
	v_fma_f32 v159, v29, v89, -v159
	v_mul_f32_e64 v160, v29, v130
	v_fma_f32 v160, v31, v131, v160
	v_fma_f32 v160, v88, v156, v160
	v_rcp_f32_e32 v160, v160
	v_cmp_ne_u32_e64 vcc, s37, v2
	v_mul_f32_e64 v160, v160, v22
	v_cndmask_b32_e64 v160, 0, v160, s[30:31]
	v_cndmask_b32_e64 v29, 0, v18, vcc
	v_cndmask_b32_e64 v145, 0, v22, s[30:31]
	v_mul_f32_e64 v139, v130, v160
	v_mul_f32_e64 v140, v131, v160
	v_mul_f32_e64 v141, v156, v160
	v_mul_f32_e64 v142, v157, v160
	v_mul_f32_e64 v143, v158, v160
	v_mul_f32_e64 v144, v159, v160
	v_add_f32_e64 v146, v125, v29
	v_mov_b32_e32 v147, v2
	ds_write_b128 v23, v[136:139]
	ds_write_b128 v23, v[140:143] offset:1024
	ds_write_b128 v23, v[144:147] offset:2048
	s_waitcnt lgkmcnt(0)
	s_barrier
	v_mov_b32_dpp v30, v36 wave_shr:1 row_mask:0xf bank_mask:0xf bound_ctrl:1
	v_mov_b32_dpp v31, v37 wave_shr:1 row_mask:0xf bank_mask:0xf bound_ctrl:1
	v_mov_b32_dpp v50, v36 wave_shl:1 row_mask:0xf bank_mask:0xf bound_ctrl:1
	v_mov_b32_dpp v51, v37 wave_shl:1 row_mask:0xf bank_mask:0xf bound_ctrl:1
	v_pk_mul_f32 v[56:57], v[36:37], v[40:41] op_sel_hi:[1,0]
	v_pk_mul_f32 v[88:89], v[36:37], v[40:41] op_sel:[0,1]
	v_pk_mul_f32 v[114:115], v[36:37], v[42:43] op_sel_hi:[1,0]
	v_pk_add_f32 v[122:123], v[36:37], v[30:31]
	v_pk_fma_f32 v[56:57], v[30:31], v[96:97], v[56:57] op_sel_hi:[1,0,1]
	v_pk_fma_f32 v[88:89], v[30:31], v[96:97], v[88:89] op_sel:[0,1,0]
	v_pk_fma_f32 v[114:115], v[30:31], v[98:99], v[114:115] op_sel_hi:[1,0,1]
	v_pk_add_f32 v[122:123], v[122:123], v[50:51]
	v_pk_fma_f32 v[56:57], v[50:51], v[100:101], v[56:57] op_sel_hi:[1,0,1]
	v_pk_fma_f32 v[88:89], v[50:51], v[100:101], v[88:89] op_sel:[0,1,0]
	v_pk_fma_f32 v[114:115], v[50:51], v[102:103], v[114:115] op_sel_hi:[1,0,1]
	v_pk_add_f32 v[30:31], v[120:121], v[122:123]
	v_pk_add_f32 v[50:51], v[134:135], v[30:31]
	v_pk_add_f32 v[120:121], v[80:81], v[56:57]
	v_pk_add_f32 v[124:125], v[110:111], v[120:121]
	v_pk_add_f32 v[80:81], v[92:93], v[88:89]
	v_pk_add_f32 v[110:111], v[116:117], v[80:81]
	v_pk_add_f32 v[92:93], v[108:109], v[114:115]
	v_pk_add_f32 v[116:117], v[132:133], v[92:93]
	v_pk_fma_f32 v[124:125], v[136:137], v[50:51], v[124:125] op_sel_hi:[0,1,1] neg_lo:[1,0,0] neg_hi:[1,0,0]
	v_pk_fma_f32 v[110:111], v[136:137], v[50:51], v[110:111] op_sel:[1,0,0] neg_lo:[1,0,0] neg_hi:[1,0,0]
	v_pk_fma_f32 v[116:117], v[138:139], v[50:51], v[116:117] op_sel_hi:[0,1,1] neg_lo:[1,0,0] neg_hi:[1,0,0]
	v_pk_mul_f32 v[108:109], v[138:139], v[124:125] op_sel:[1,0]
	v_pk_mul_f32 v[126:127], v[140:141], v[124:125] op_sel_hi:[0,1]
	v_pk_mul_f32 v[130:131], v[140:141], v[124:125] op_sel:[1,0]
	v_pk_fma_f32 v[108:109], v[140:141], v[110:111], v[108:109] op_sel_hi:[0,1,1]
	v_pk_fma_f32 v[126:127], v[142:143], v[110:111], v[126:127] op_sel_hi:[0,1,1]
	v_pk_fma_f32 v[130:131], v[142:143], v[110:111], v[130:131] op_sel:[1,0,0]
	v_pk_fma_f32 v[108:109], v[140:141], v[116:117], v[108:109] op_sel:[1,0,0]
	v_pk_fma_f32 v[126:127], v[142:143], v[116:117], v[126:127] op_sel:[1,0,0]
	v_pk_fma_f32 v[130:131], v[144:145], v[116:117], v[130:131] op_sel_hi:[0,1,1]
	v_pk_mul_f32 v[132:133], v[136:137], v[108:109] op_sel_hi:[0,1]
	v_pk_fma_f32 v[132:133], v[136:137], v[126:127], v[132:133] op_sel:[1,0,0]
	v_pk_fma_f32 v[132:133], v[138:139], v[130:131], v[132:133] op_sel_hi:[0,1,1]
	v_pk_fma_f32 v[132:133], v[144:145], v[50:51], v[132:133] op_sel:[1,0,0] neg_lo:[0,0,1] neg_hi:[0,0,1]
	v_cmp_eq_u32_e64 s[10:11], 6, v147
	v_cmp_eq_u32_e64 s[14:15], 7, v147
	v_pk_add_f32 v[50:51], v[90:91], v[108:109]
	v_pk_add_f32 v[110:111], v[94:95], v[50:51]
	v_pk_add_f32 v[90:91], v[118:119], v[126:127]
	v_pk_add_f32 v[94:95], v[128:129], v[90:91]
	v_pk_add_f32 v[116:117], v[152:153], v[130:131]
	v_pk_add_f32 v[118:119], v[148:149], v[116:117]
	v_pk_add_f32 v[124:125], v[154:155], v[132:133]
	v_pk_add_f32 v[128:129], v[150:151], v[124:125]
	v_pk_fma_f32 v[134:135], v[44:45], v[110:111], v[128:129] op_sel_hi:[0,1,1]
	v_pk_fma_f32 v[148:149], v[68:69], v[110:111], v[128:129] op_sel_hi:[0,1,1]
	v_pk_fma_f32 v[134:135], v[44:45], v[94:95], v[134:135] op_sel:[1,0,0]
	v_pk_fma_f32 v[148:149], v[68:69], v[94:95], v[148:149] op_sel:[1,0,0]
	v_pk_fma_f32 v[134:135], v[46:47], v[118:119], v[134:135] op_sel_hi:[0,1,1]
	v_pk_fma_f32 v[148:149], v[70:71], v[118:119], v[148:149] op_sel_hi:[0,1,1]
	v_pk_fma_f32 v[128:129], v[12:13], v[110:111], v[128:129] op_sel_hi:[0,1,1]
	v_pk_fma_f32 v[128:129], v[12:13], v[94:95], v[128:129] op_sel:[1,0,0]
	v_pk_fma_f32 v[128:129], v[14:15], v[118:119], v[128:129] op_sel_hi:[0,1,1]
	v_cndmask_b32_e64 v150, 0, v18, s[10:11]
	v_cndmask_b32_e64 v151, 0, v18, s[14:15]
	v_add_f32_dpp v128, v134, v128 wave_shl:1 row_mask:0xf bank_mask:0xf bound_ctrl:1
	v_add_f32_dpp v129, v135, v129 wave_shl:1 row_mask:0xf bank_mask:0xf bound_ctrl:1
	s_add_i32 s4, s34, 4
	s_cmpk_lt_i32 s4, 0x201
	s_cselect_b64 s[12:13], s[0:1], 0
	v_add_f32_dpp v128, v148, v128 wave_shr:1 row_mask:0xf bank_mask:0xf bound_ctrl:1
	v_add_f32_dpp v129, v149, v129 wave_shr:1 row_mask:0xf bank_mask:0xf bound_ctrl:1
	v_pk_fma_f32 v[128:129], v[6:7], v[146:147], v[128:129] op_sel_hi:[1,0,1] neg_lo:[0,0,1] neg_hi:[0,0,1]
	v_pk_add_f32 v[128:129], v[128:129], v[150:151] neg_lo:[0,1] neg_hi:[0,1]
	v_pk_mul_f32 v[152:153], v[128:129], v[128:129]
	v_add_f32_e32 v152, v152, v153
	v_cndmask_b32_e64 v153, 0, v152, s[12:13]
	v_add_f32_e32 v1, v1, v153
	s_add_i32 s5, s34, 9
	s_min_i32 s5, s5, 0x200
	s_mul_i32 s6, s5, 0x804
	s_add_i32 s6, s6, s35
	s_add_i32 s7, s6, 0x505014
	s_add_i32 s8, s6, 0x606018
	s_mul_i32 s9, s5, 0x180c
	s_add_i32 s9, s9, s33
	s_add_i32 s4, s34, 10
	s_min_i32 s4, s4, 0x200
	s_mul_i32 s4, s4, 0x804
	s_add_i32 s4, s4, s38
	buffer_load_dword v2, v28, s[20:23], s4 offen nt
	buffer_load_dwordx3 v[12:14], v27, s[24:27], s9 offen nt
	buffer_load_dword v6, v28, s[16:19], s7 offen nt
	buffer_load_dword v7, v28, s[16:19], s8 offen nt
	s_waitcnt vmcnt(8)
	v_mov_b32_dpp v44, v72 wave_shr:1 row_mask:0xf bank_mask:0xf bound_ctrl:1
	v_mov_b32_dpp v45, v73 wave_shr:1 row_mask:0xf bank_mask:0xf bound_ctrl:1
	v_mov_b32_dpp v46, v74 wave_shr:1 row_mask:0xf bank_mask:0xf bound_ctrl:1
	v_mov_b32_dpp v68, v72 wave_shl:1 row_mask:0xf bank_mask:0xf bound_ctrl:1
	v_mov_b32_dpp v69, v73 wave_shl:1 row_mask:0xf bank_mask:0xf bound_ctrl:1
	v_mov_b32_dpp v70, v74 wave_shl:1 row_mask:0xf bank_mask:0xf bound_ctrl:1
	s_add_i32 s4, s34, 8
	s_cmpk_lt_u32 s4, 0x201
	s_cselect_b64 s[12:13], s[40:41], 0
	v_cmp_eq_u32_e64 s[14:15], s37, v24
	s_and_b64 s[14:15], s[14:15], s[12:13]
	v_cndmask_b32_e64 v29, 0, 1, s[14:15]
	v_mul_f32_e64 v94, v72, v72
	v_mul_f32_e64 v95, v72, v73
	v_mul_f32_e64 v110, v72, v74
	v_mul_f32_e64 v111, v73, v73
	v_mul_f32_e64 v118, v73, v74
	v_mul_f32_e64 v119, v74, v74
	v_or_b32_dpp v128, v29, v29 wave_shr:1 row_mask:0xf bank_mask:0xf bound_ctrl:1
	s_nop 1
	v_or_b32_dpp v128, v29, v128 wave_shl:1 row_mask:0xf bank_mask:0xf bound_ctrl:1
	s_nop 1
	v_or_b32_dpp v129, v128, v128 wave_shr:1 row_mask:0xf bank_mask:0xf bound_ctrl:1
	s_nop 1
	v_or_b32_dpp v129, v128, v129 wave_shl:1 row_mask:0xf bank_mask:0xf bound_ctrl:1
	v_or3_b32 v29, v129, v53, v84
	v_or3_b32 v29, v29, v85, v52
	s_add_i32 s4, s34, 5
	s_cmpk_lt_u32 s4, 0x1ff
	s_cselect_b64 s[12:13], s[42:43], 0
	v_cmp_ne_u32_e64 s[30:31], 0, v29
	s_and_b64 s[30:31], s[30:31], s[12:13]
	v_cndmask_b32_e64 v29, 0, 1.0, s[30:31]
	v_add_f32_e64 v134, v72, v44
	v_add_f32_e64 v135, v73, v45
	v_add_f32_e64 v136, v74, v46
	v_fma_f32 v94, v44, v44, v94
	v_fma_f32 v95, v44, v45, v95
	v_fma_f32 v110, v44, v46, v110
	v_fma_f32 v111, v45, v45, v111
	v_fma_f32 v118, v45, v46, v118
	v_fma_f32 v119, v46, v46, v119
	v_add_f32_dpp v143, v29, v29 wave_shr:1 row_mask:0xf bank_mask:0xf bound_ctrl:1
	v_add_f32_e64 v134, v134, v68
	v_add_f32_e64 v135, v135, v69
	v_add_f32_e64 v136, v136, v70
	v_fma_f32 v137, v68, v68, v94
	v_fma_f32 v138, v68, v69, v95
	v_fma_f32 v139, v68, v70, v110
	v_fma_f32 v140, v69, v69, v111
	v_fma_f32 v141, v69, v70, v118
	v_fma_f32 v142, v70, v70, v119
	v_add_f32_dpp v143, v29, v143 wave_shl:1 row_mask:0xf bank_mask:0xf bound_ctrl:1
	v_pk_add_f32 v[94:95], v[38:39], v[134:135]
	v_pk_add_f32 v[38:39], v[54:55], v[136:137]
	v_pk_add_f32 v[54:55], v[62:63], v[138:139]
	v_pk_add_f32 v[62:63], v[66:67], v[140:141]
	v_pk_add_f32 v[66:67], v[86:87], v[142:143]
	v_mul_f32_e64 v144, v94, v22
	v_mul_f32_e64 v145, v95, v22
	v_mul_f32_e64 v146, v38, v22
	v_fma_f32 v29, v39, v22, v26
	v_mul_f32_e64 v128, v54, v22
	v_mul_f32_e64 v86, v55, v22
	v_fma_f32 v87, v62, v22, v26
	v_mul_f32_e64 v110, v63, v22
	v_fma_f32 v111, v66, v22, v26
	v_fma_f32 v29, -v144, v144, v29
	v_fma_f32 v128, -v144, v145, v128
	v_fma_f32 v86, -v144, v146, v86
	v_fma_f32 v87, -v145, v145, v87
	v_fma_f32 v110, -v145, v146, v110
	v_fma_f32 v111, -v146, v146, v111
	v_mul_f32_e64 v118, v110, v110
	v_mul_f32_e64 v119, v128, v111
	v_mul_f32_e64 v156, v86, v87
	v_mul_f32_e64 v157, v86, v86
	v_mul_f32_e64 v158, v29, v110
	v_mul_f32_e64 v159, v128, v128
	v_fma_f32 v118, v87, v111, -v118
	v_fma_f32 v119, v86, v110, -v119
	v_fma_f32 v156, v128, v110, -v156
	v_fma_f32 v157, v29, v111, -v157
	v_fma_f32 v158, v128, v86, -v158
	v_fma_f32 v159, v29, v87, -v159
	v_mul_f32_e64 v160, v29, v118
	v_fma_f32 v160, v128, v119, v160
	v_fma_f32 v160, v86, v156, v160
	v_rcp_f32_e32 v160, v160
	v_cmp_ne_u32_e64 vcc, s37, v3
	v_mul_f32_e64 v160, v160, v22
	v_cndmask_b32_e64 v160, 0, v160, s[30:31]
	v_cndmask_b32_e64 v29, 0, v18, vcc
	v_cndmask_b32_e64 v153, 0, v22, s[30:31]
	v_mul_f32_e64 v147, v118, v160
	v_mul_f32_e64 v148, v119, v160
	v_mul_f32_e64 v149, v156, v160
	v_mul_f32_e64 v150, v157, v160
	v_mul_f32_e64 v151, v158, v160
	v_mul_f32_e64 v152, v159, v160
	v_add_f32_e64 v154, v67, v29
	v_mov_b32_e32 v155, v3
	ds_write_b128 v23, v[144:147] offset:3072
	ds_write_b128 v23, v[148:151] offset:4096
	ds_write_b128 v23, v[152:155] offset:5120
	s_waitcnt lgkmcnt(0)
	s_barrier
	v_mov_b32_dpp v38, v48 wave_shr:1 row_mask:0xf bank_mask:0xf bound_ctrl:1
	v_mov_b32_dpp v39, v49 wave_shr:1 row_mask:0xf bank_mask:0xf bound_ctrl:1
	v_mov_b32_dpp v54, v48 wave_shl:1 row_mask:0xf bank_mask:0xf bound_ctrl:1
	v_mov_b32_dpp v55, v49 wave_shl:1 row_mask:0xf bank_mask:0xf bound_ctrl:1
	v_pk_mul_f32 v[62:63], v[48:49], v[72:73] op_sel_hi:[1,0]
	v_pk_mul_f32 v[66:67], v[48:49], v[72:73] op_sel:[0,1]
	v_pk_mul_f32 v[86:87], v[48:49], v[74:75] op_sel_hi:[1,0]
	v_pk_add_f32 v[94:95], v[48:49], v[38:39]
	v_pk_fma_f32 v[62:63], v[38:39], v[44:45], v[62:63] op_sel_hi:[1,0,1]
	v_pk_fma_f32 v[66:67], v[38:39], v[44:45], v[66:67] op_sel:[0,1,0]
	v_pk_fma_f32 v[86:87], v[38:39], v[46:47], v[86:87] op_sel_hi:[1,0,1]
	v_pk_add_f32 v[94:95], v[94:95], v[54:55]
	v_pk_fma_f32 v[62:63], v[54:55], v[68:69], v[62:63] op_sel_hi:[1,0,1]
	v_pk_fma_f32 v[66:67], v[54:55], v[68:69], v[66:67] op_sel:[0,1,0]
	v_pk_fma_f32 v[86:87], v[54:55], v[70:71], v[86:87] op_sel_hi:[1,0,1]
	v_pk_add_f32 v[38:39], v[30:31], v[94:95]
	v_pk_add_f32 v[30:31], v[120:121], v[62:63]
	v_pk_add_f32 v[54:55], v[80:81], v[66:67]
	v_pk_add_f32 v[80:81], v[92:93], v[86:87]
	v_pk_fma_f32 v[30:31], v[144:145], v[38:39], v[30:31] op_sel_hi:[0,1,1] neg_lo:[1,0,0] neg_hi:[1,0,0]
	v_pk_fma_f32 v[54:55], v[144:145], v[38:39], v[54:55] op_sel:[1,0,0] neg_lo:[1,0,0] neg_hi:[1,0,0]
	v_pk_fma_f32 v[80:81], v[146:147], v[38:39], v[80:81] op_sel_hi:[0,1,1] neg_lo:[1,0,0] neg_hi:[1,0,0]
	v_pk_mul_f32 v[92:93], v[146:147], v[30:31] op_sel:[1,0]
	v_pk_mul_f32 v[110:111], v[148:149], v[30:31] op_sel_hi:[0,1]
	v_pk_mul_f32 v[118:119], v[148:149], v[30:31] op_sel:[1,0]
	v_pk_fma_f32 v[92:93], v[148:149], v[54:55], v[92:93] op_sel_hi:[0,1,1]
	v_pk_fma_f32 v[110:111], v[150:151], v[54:55], v[110:111] op_sel_hi:[0,1,1]
	v_pk_fma_f32 v[118:119], v[150:151], v[54:55], v[118:119] op_sel:[1,0,0]
	v_pk_fma_f32 v[92:93], v[148:149], v[80:81], v[92:93] op_sel:[1,0,0]
	v_pk_fma_f32 v[110:111], v[150:151], v[80:81], v[110:111] op_sel:[1,0,0]
	v_pk_fma_f32 v[118:119], v[152:153], v[80:81], v[118:119] op_sel_hi:[0,1,1]
	v_pk_mul_f32 v[120:121], v[144:145], v[92:93] op_sel_hi:[0,1]
	v_pk_fma_f32 v[120:121], v[144:145], v[110:111], v[120:121] op_sel:[1,0,0]
	v_pk_fma_f32 v[120:121], v[146:147], v[118:119], v[120:121] op_sel_hi:[0,1,1]
	v_pk_fma_f32 v[120:121], v[152:153], v[38:39], v[120:121] op_sel:[1,0,0] neg_lo:[0,0,1] neg_hi:[0,0,1]
	v_cmp_eq_u32_e64 s[10:11], 6, v155
	v_cmp_eq_u32_e64 s[14:15], 7, v155
	v_pk_add_f32 v[30:31], v[50:51], v[92:93]
	v_pk_add_f32 v[38:39], v[90:91], v[110:111]
	v_pk_add_f32 v[50:51], v[116:117], v[118:119]
	v_pk_add_f32 v[54:55], v[124:125], v[120:121]
	v_pk_fma_f32 v[80:81], v[76:77], v[30:31], v[54:55] op_sel_hi:[0,1,1]
	v_pk_fma_f32 v[90:91], v[104:105], v[30:31], v[54:55] op_sel_hi:[0,1,1]
	v_pk_fma_f32 v[80:81], v[76:77], v[38:39], v[80:81] op_sel:[1,0,0]
	v_pk_fma_f32 v[90:91], v[104:105], v[38:39], v[90:91] op_sel:[1,0,0]
	v_pk_fma_f32 v[80:81], v[78:79], v[50:51], v[80:81] op_sel_hi:[0,1,1]
	v_pk_fma_f32 v[90:91], v[106:107], v[50:51], v[90:91] op_sel_hi:[0,1,1]
	v_pk_fma_f32 v[54:55], v[32:33], v[30:31], v[54:55] op_sel_hi:[0,1,1]
	v_pk_fma_f32 v[54:55], v[32:33], v[38:39], v[54:55] op_sel:[1,0,0]
	v_pk_fma_f32 v[54:55], v[34:35], v[50:51], v[54:55] op_sel_hi:[0,1,1]
	v_cndmask_b32_e64 v116, 0, v18, s[10:11]
	v_cndmask_b32_e64 v117, 0, v18, s[14:15]
	v_add_f32_dpp v54, v80, v54 wave_shl:1 row_mask:0xf bank_mask:0xf bound_ctrl:1
	v_add_f32_dpp v55, v81, v55 wave_shl:1 row_mask:0xf bank_mask:0xf bound_ctrl:1
	s_add_i32 s4, s34, 5
	s_cmpk_lt_i32 s4, 0x201
	s_cselect_b64 s[12:13], s[0:1], 0
	v_add_f32_dpp v54, v90, v54 wave_shr:1 row_mask:0xf bank_mask:0xf bound_ctrl:1
	v_add_f32_dpp v55, v91, v55 wave_shr:1 row_mask:0xf bank_mask:0xf bound_ctrl:1
	v_pk_fma_f32 v[54:55], v[20:21], v[154:155], v[54:55] op_sel_hi:[1,0,1] neg_lo:[0,0,1] neg_hi:[0,0,1]
	v_pk_add_f32 v[54:55], v[54:55], v[116:117] neg_lo:[0,1] neg_hi:[0,1]
	v_pk_mul_f32 v[124:125], v[54:55], v[54:55]
	v_add_f32_e32 v124, v124, v125
	v_cndmask_b32_e64 v125, 0, v124, s[12:13]
	v_add_f32_e32 v1, v1, v125
	s_add_i32 s5, s34, 10
	s_min_i32 s5, s5, 0x200
	s_mul_i32 s6, s5, 0x804
	s_add_i32 s6, s6, s35
	s_add_i32 s7, s6, 0x505014
	s_add_i32 s8, s6, 0x606018
	s_mul_i32 s9, s5, 0x180c
	s_add_i32 s9, s9, s33
	s_add_i32 s4, s34, 11
	s_min_i32 s4, s4, 0x200
	s_mul_i32 s4, s4, 0x804
	s_add_i32 s4, s4, s38
	buffer_load_dword v3, v28, s[20:23], s4 offen nt
	buffer_load_dwordx3 v[32:34], v27, s[24:27], s9 offen nt
	buffer_load_dword v20, v28, s[16:19], s7 offen nt
	buffer_load_dword v21, v28, s[16:19], s8 offen nt
	s_waitcnt vmcnt(8)
	v_mov_b32_dpp v76, v8 wave_shr:1 row_mask:0xf bank_mask:0xf bound_ctrl:1
	v_mov_b32_dpp v77, v9 wave_shr:1 row_mask:0xf bank_mask:0xf bound_ctrl:1
	v_mov_b32_dpp v78, v10 wave_shr:1 row_mask:0xf bank_mask:0xf bound_ctrl:1
	v_mov_b32_dpp v104, v8 wave_shl:1 row_mask:0xf bank_mask:0xf bound_ctrl:1
	v_mov_b32_dpp v105, v9 wave_shl:1 row_mask:0xf bank_mask:0xf bound_ctrl:1
	v_mov_b32_dpp v106, v10 wave_shl:1 row_mask:0xf bank_mask:0xf bound_ctrl:1
	s_add_i32 s4, s34, 9
	s_cmpk_lt_u32 s4, 0x201
	s_cselect_b64 s[12:13], s[40:41], 0
	v_cmp_eq_u32_e64 s[14:15], s37, v17
	s_and_b64 s[14:15], s[14:15], s[12:13]
	v_cndmask_b32_e64 v29, 0, 1, s[14:15]
	v_mul_f32_e64 v30, v8, v8
	v_mul_f32_e64 v31, v8, v9
	v_mul_f32_e64 v38, v8, v10
	v_mul_f32_e64 v39, v9, v9
	v_mul_f32_e64 v50, v9, v10
	v_mul_f32_e64 v51, v10, v10
	v_or_b32_dpp v52, v29, v29 wave_shr:1 row_mask:0xf bank_mask:0xf bound_ctrl:1
	s_nop 1
	v_or_b32_dpp v52, v29, v52 wave_shl:1 row_mask:0xf bank_mask:0xf bound_ctrl:1
	s_nop 1
	v_or_b32_dpp v128, v52, v52 wave_shr:1 row_mask:0xf bank_mask:0xf bound_ctrl:1
	s_nop 1
	v_or_b32_dpp v128, v52, v128 wave_shl:1 row_mask:0xf bank_mask:0xf bound_ctrl:1
	v_or3_b32 v29, v128, v129, v53
	v_or3_b32 v29, v29, v84, v85
	s_add_i32 s4, s34, 6
	s_cmpk_lt_u32 s4, 0x1ff
	s_cselect_b64 s[12:13], s[42:43], 0
	v_cmp_ne_u32_e64 s[30:31], 0, v29
	s_and_b64 s[30:31], s[30:31], s[12:13]
	v_cndmask_b32_e64 v29, 0, 1.0, s[30:31]
	v_add_f32_e64 v54, v8, v76
	v_add_f32_e64 v55, v9, v77
	v_add_f32_e64 v80, v10, v78
	v_fma_f32 v30, v76, v76, v30
	v_fma_f32 v31, v76, v77, v31
	v_fma_f32 v38, v76, v78, v38
	v_fma_f32 v39, v77, v77, v39
	v_fma_f32 v50, v77, v78, v50
	v_fma_f32 v51, v78, v78, v51
	v_add_f32_dpp v125, v29, v29 wave_shr:1 row_mask:0xf bank_mask:0xf bound_ctrl:1
	v_add_f32_e64 v54, v54, v104
	v_add_f32_e64 v55, v55, v105
	v_add_f32_e64 v80, v80, v106
	v_fma_f32 v81, v104, v104, v30
	v_fma_f32 v90, v104, v105, v31
	v_fma_f32 v91, v104, v106, v38
	v_fma_f32 v116, v105, v105, v39
	v_fma_f32 v117, v105, v106, v50
	v_fma_f32 v124, v106, v106, v51
	v_add_f32_dpp v125, v29, v125 wave_shl:1 row_mask:0xf bank_mask:0xf bound_ctrl:1
	v_pk_add_f32 v[30:31], v[134:135], v[54:55]
	v_pk_add_f32 v[38:39], v[58:59], v[30:31]
	v_pk_add_f32 v[50:51], v[136:137], v[80:81]
	v_pk_add_f32 v[58:59], v[60:61], v[50:51]
	v_pk_add_f32 v[60:61], v[138:139], v[90:91]
	v_pk_add_f32 v[134:135], v[64:65], v[60:61]
	v_pk_add_f32 v[64:65], v[140:141], v[116:117]
	v_pk_add_f32 v[136:137], v[82:83], v[64:65]
	v_pk_add_f32 v[82:83], v[142:143], v[124:125]
	v_pk_add_f32 v[138:139], v[112:113], v[82:83]
	v_mul_f32_e64 v140, v38, v22
	v_mul_f32_e64 v141, v39, v22
	v_mul_f32_e64 v142, v58, v22
	v_fma_f32 v29, v59, v22, v26
	v_mul_f32_e64 v52, v134, v22
	v_mul_f32_e64 v112, v135, v22
	v_fma_f32 v113, v136, v22, v26
	v_mul_f32_e64 v152, v137, v22
	v_fma_f32 v153, v138, v22, v26
	v_fma_f32 v29, -v140, v140, v29
	v_fma_f32 v52, -v140, v141, v52
	v_fma_f32 v112, -v140, v142, v112
	v_fma_f32 v113, -v141, v141, v113
	v_fma_f32 v152, -v141, v142, v152
	v_fma_f32 v153, -v142, v142, v153
	v_mul_f32_e64 v154, v152, v152
	v_mul_f32_e64 v155, v52, v153
	v_mul_f32_e64 v156, v112, v113
	v_mul_f32_e64 v157, v112, v112
	v_mul_f32_e64 v158, v29, v152
	v_mul_f32_e64 v159, v52, v52
	v_fma_f32 v154, v113, v153, -v154
	v_fma_f32 v155, v112, v152, -v155
	v_fma_f32 v156, v52, v152, -v156
	v_fma_f32 v157, v29, v153, -v157
	v_fma_f32 v158, v52, v112, -v158
	v_fma_f32 v159, v29, v113, -v159
	v_mul_f32_e64 v160, v29, v154
	v_fma_f32 v160, v52, v155, v160
	v_fma_f32 v160, v112, v156, v160
	v_rcp_f32_e32 v160, v160
	v_cmp_ne_u32_e64 vcc, s37, v16
	v_mul_f32_e64 v160, v160, v22
	v_cndmask_b32_e64 v160, 0, v160, s[30:31]
	v_cndmask_b32_e64 v29, 0, v18, vcc
	v_cndmask_b32_e64 v149, 0, v22, s[30:31]
	v_mul_f32_e64 v143, v154, v160
	v_mul_f32_e64 v144, v155, v160
	v_mul_f32_e64 v145, v156, v160
	v_mul_f32_e64 v146, v157, v160
	v_mul_f32_e64 v147, v158, v160
	v_mul_f32_e64 v148, v159, v160
	v_add_f32_e64 v150, v139, v29
	v_mov_b32_e32 v151, v16
	ds_write_b128 v23, v[140:143]
	ds_write_b128 v23, v[144:147] offset:1024
	ds_write_b128 v23, v[148:151] offset:2048
	s_waitcnt lgkmcnt(0)
	s_barrier
	v_mov_b32_dpp v38, v4 wave_shr:1 row_mask:0xf bank_mask:0xf bound_ctrl:1
	v_mov_b32_dpp v39, v5 wave_shr:1 row_mask:0xf bank_mask:0xf bound_ctrl:1
	v_mov_b32_dpp v58, v4 wave_shl:1 row_mask:0xf bank_mask:0xf bound_ctrl:1
	v_mov_b32_dpp v59, v5 wave_shl:1 row_mask:0xf bank_mask:0xf bound_ctrl:1
	v_pk_mul_f32 v[112:113], v[4:5], v[8:9] op_sel_hi:[1,0]
	v_pk_mul_f32 v[134:135], v[4:5], v[8:9] op_sel:[0,1]
	v_pk_mul_f32 v[136:137], v[4:5], v[10:11] op_sel_hi:[1,0]
	v_pk_add_f32 v[138:139], v[4:5], v[38:39]
	v_pk_fma_f32 v[112:113], v[38:39], v[76:77], v[112:113] op_sel_hi:[1,0,1]
	v_pk_fma_f32 v[134:135], v[38:39], v[76:77], v[134:135] op_sel:[0,1,0]
	v_pk_fma_f32 v[136:137], v[38:39], v[78:79], v[136:137] op_sel_hi:[1,0,1]
	v_pk_add_f32 v[138:139], v[138:139], v[58:59]
	v_pk_fma_f32 v[112:113], v[58:59], v[104:105], v[112:113] op_sel_hi:[1,0,1]
	v_pk_fma_f32 v[134:135], v[58:59], v[104:105], v[134:135] op_sel:[0,1,0]
	v_pk_fma_f32 v[136:137], v[58:59], v[106:107], v[136:137] op_sel_hi:[1,0,1]
	v_pk_add_f32 v[38:39], v[94:95], v[138:139]
	v_pk_add_f32 v[58:59], v[122:123], v[38:39]
	v_pk_add_f32 v[94:95], v[62:63], v[112:113]
	v_pk_add_f32 v[122:123], v[56:57], v[94:95]
	v_pk_add_f32 v[56:57], v[66:67], v[134:135]
	v_pk_add_f32 v[62:63], v[88:89], v[56:57]
	v_pk_add_f32 v[66:67], v[86:87], v[136:137]
	v_pk_add_f32 v[88:89], v[114:115], v[66:67]
	v_pk_fma_f32 v[122:123], v[140:141], v[58:59], v[122:123] op_sel_hi:[0,1,1] neg_lo:[1,0,0] neg_hi:[1,0,0]
	v_pk_fma_f32 v[62:63], v[140:141], v[58:59], v[62:63] op_sel:[1,0,0] neg_lo:[1,0,0] neg_hi:[1,0,0]
	v_pk_fma_f32 v[88:89], v[142:143], v[58:59], v[88:89] op_sel_hi:[0,1,1] neg_lo:[1,0,0] neg_hi:[1,0,0]
	v_pk_mul_f32 v[86:87], v[142:143], v[122:123] op_sel:[1,0]
	v_pk_mul_f32 v[114:115], v[144:145], v[122:123] op_sel_hi:[0,1]
	v_pk_mul_f32 v[152:153], v[144:145], v[122:123] op_sel:[1,0]
	v_pk_fma_f32 v[86:87], v[144:145], v[62:63], v[86:87] op_sel_hi:[0,1,1]
	v_pk_fma_f32 v[114:115], v[146:147], v[62:63], v[114:115] op_sel_hi:[0,1,1]
	v_pk_fma_f32 v[152:153], v[146:147], v[62:63], v[152:153] op_sel:[1,0,0]
	v_pk_fma_f32 v[86:87], v[144:145], v[88:89], v[86:87] op_sel:[1,0,0]
	v_pk_fma_f32 v[114:115], v[146:147], v[88:89], v[114:115] op_sel:[1,0,0]
	v_pk_fma_f32 v[152:153], v[148:149], v[88:89], v[152:153] op_sel_hi:[0,1,1]
	v_pk_mul_f32 v[154:155], v[140:141], v[86:87] op_sel_hi:[0,1]
	v_pk_fma_f32 v[154:155], v[140:141], v[114:115], v[154:155] op_sel:[1,0,0]
	v_pk_fma_f32 v[154:155], v[142:143], v[152:153], v[154:155] op_sel_hi:[0,1,1]
	v_pk_fma_f32 v[154:155], v[148:149], v[58:59], v[154:155] op_sel:[1,0,0] neg_lo:[0,0,1] neg_hi:[0,0,1]
	v_cmp_eq_u32_e64 s[10:11], 6, v151
	v_cmp_eq_u32_e64 s[14:15], 7, v151
	v_pk_add_f32 v[58:59], v[92:93], v[86:87]
	v_pk_add_f32 v[62:63], v[108:109], v[58:59]
	v_pk_add_f32 v[88:89], v[110:111], v[114:115]
	v_pk_add_f32 v[92:93], v[126:127], v[88:89]
	v_pk_add_f32 v[108:109], v[118:119], v[152:153]
	v_pk_add_f32 v[110:111], v[130:131], v[108:109]
	v_pk_add_f32 v[118:119], v[120:121], v[154:155]
	v_pk_add_f32 v[122:123], v[132:133], v[118:119]
	v_pk_fma_f32 v[120:121], v[96:97], v[62:63], v[122:123] op_sel_hi:[0,1,1]
	v_pk_fma_f32 v[126:127], v[100:101], v[62:63], v[122:123] op_sel_hi:[0,1,1]
	v_pk_fma_f32 v[120:121], v[96:97], v[92:93], v[120:121] op_sel:[1,0,0]
	v_pk_fma_f32 v[126:127], v[100:101], v[92:93], v[126:127] op_sel:[1,0,0]
	v_pk_fma_f32 v[120:121], v[98:99], v[110:111], v[120:121] op_sel_hi:[0,1,1]
	v_pk_fma_f32 v[126:127], v[102:103], v[110:111], v[126:127] op_sel_hi:[0,1,1]
	v_pk_fma_f32 v[122:123], v[40:41], v[62:63], v[122:123] op_sel_hi:[0,1,1]
	v_pk_fma_f32 v[122:123], v[40:41], v[92:93], v[122:123] op_sel:[1,0,0]
	v_pk_fma_f32 v[122:123], v[42:43], v[110:111], v[122:123] op_sel_hi:[0,1,1]
	v_cndmask_b32_e64 v130, 0, v18, s[10:11]
	v_cndmask_b32_e64 v131, 0, v18, s[14:15]
	v_add_f32_dpp v122, v120, v122 wave_shl:1 row_mask:0xf bank_mask:0xf bound_ctrl:1
	v_add_f32_dpp v123, v121, v123 wave_shl:1 row_mask:0xf bank_mask:0xf bound_ctrl:1
	s_add_i32 s4, s34, 6
	s_cmpk_lt_i32 s4, 0x201
	s_cselect_b64 s[12:13], s[0:1], 0
	v_add_f32_dpp v122, v126, v122 wave_shr:1 row_mask:0xf bank_mask:0xf bound_ctrl:1
	v_add_f32_dpp v123, v127, v123 wave_shr:1 row_mask:0xf bank_mask:0xf bound_ctrl:1
	v_pk_fma_f32 v[122:123], v[36:37], v[150:151], v[122:123] op_sel_hi:[1,0,1] neg_lo:[0,0,1] neg_hi:[0,0,1]
	v_pk_add_f32 v[122:123], v[122:123], v[130:131] neg_lo:[0,1] neg_hi:[0,1]
	v_pk_mul_f32 v[132:133], v[122:123], v[122:123]
	v_add_f32_e32 v132, v132, v133
	v_cndmask_b32_e64 v133, 0, v132, s[12:13]
	v_add_f32_e32 v1, v1, v133
	s_add_i32 s5, s34, 11
	s_min_i32 s5, s5, 0x200
	s_mul_i32 s6, s5, 0x804
	s_add_i32 s6, s6, s35
	s_add_i32 s7, s6, 0x505014
	s_add_i32 s8, s6, 0x606018
	s_mul_i32 s9, s5, 0x180c
	s_add_i32 s9, s9, s33
	s_add_i32 s4, s34, 12
	s_min_i32 s4, s4, 0x200
	s_mul_i32 s4, s4, 0x804
	s_add_i32 s4, s4, s38
	buffer_load_dword v16, v28, s[20:23], s4 offen nt
	buffer_load_dwordx3 v[40:42], v27, s[24:27], s9 offen nt
	buffer_load_dword v36, v28, s[16:19], s7 offen nt
	buffer_load_dword v37, v28, s[16:19], s8 offen nt
	s_waitcnt vmcnt(8)
	v_mov_b32_dpp v96, v12 wave_shr:1 row_mask:0xf bank_mask:0xf bound_ctrl:1
	v_mov_b32_dpp v97, v13 wave_shr:1 row_mask:0xf bank_mask:0xf bound_ctrl:1
	v_mov_b32_dpp v98, v14 wave_shr:1 row_mask:0xf bank_mask:0xf bound_ctrl:1
	v_mov_b32_dpp v100, v12 wave_shl:1 row_mask:0xf bank_mask:0xf bound_ctrl:1
	v_mov_b32_dpp v101, v13 wave_shl:1 row_mask:0xf bank_mask:0xf bound_ctrl:1
	v_mov_b32_dpp v102, v14 wave_shl:1 row_mask:0xf bank_mask:0xf bound_ctrl:1
	s_add_i32 s4, s34, 10
	s_cmpk_lt_u32 s4, 0x201
	s_cselect_b64 s[12:13], s[40:41], 0
	v_cmp_eq_u32_e64 s[14:15], s37, v2
	s_and_b64 s[14:15], s[14:15], s[12:13]
	v_cndmask_b32_e64 v29, 0, 1, s[14:15]
	v_mul_f32_e64 v62, v12, v12
	v_mul_f32_e64 v63, v12, v13
	v_mul_f32_e64 v92, v12, v14
	v_mul_f32_e64 v93, v13, v13
	v_mul_f32_e64 v110, v13, v14
	v_mul_f32_e64 v111, v14, v14
	v_or_b32_dpp v52, v29, v29 wave_shr:1 row_mask:0xf bank_mask:0xf bound_ctrl:1
	s_nop 1
	v_or_b32_dpp v52, v29, v52 wave_shl:1 row_mask:0xf bank_mask:0xf bound_ctrl:1
	s_nop 1
	v_or_b32_dpp v85, v52, v52 wave_shr:1 row_mask:0xf bank_mask:0xf bound_ctrl:1
	s_nop 1
	v_or_b32_dpp v85, v52, v85 wave_shl:1 row_mask:0xf bank_mask:0xf bound_ctrl:1
	v_or3_b32 v29, v85, v128, v129
	v_or3_b32 v29, v29, v53, v84
	s_add_i32 s4, s34, 7
	s_cmpk_lt_u32 s4, 0x1ff
	s_cselect_b64 s[12:13], s[42:43], 0
	v_cmp_ne_u32_e64 s[30:31], 0, v29
	s_and_b64 s[30:31], s[30:31], s[12:13]
	v_cndmask_b32_e64 v29, 0, 1.0, s[30:31]
	v_add_f32_e64 v120, v12, v96
	v_add_f32_e64 v121, v13, v97
	v_add_f32_e64 v122, v14, v98
	v_fma_f32 v62, v96, v96, v62
	v_fma_f32 v63, v96, v97, v63
	v_fma_f32 v92, v96, v98, v92
	v_fma_f32 v93, v97, v97, v93
	v_fma_f32 v110, v97, v98, v110
	v_fma_f32 v111, v98, v98, v111
	v_add_f32_dpp v133, v29, v29 wave_shr:1 row_mask:0xf bank_mask:0xf bound_ctrl:1
	v_add_f32_e64 v120, v120, v100
	v_add_f32_e64 v121, v121, v101
	v_add_f32_e64 v122, v122, v102
	v_fma_f32 v123, v100, v100, v62
	v_fma_f32 v126, v100, v101, v63
	v_fma_f32 v127, v100, v102, v92
	v_fma_f32 v130, v101, v101, v93
	v_fma_f32 v131, v101, v102, v110
	v_fma_f32 v132, v102, v102, v111
	v_add_f32_dpp v133, v29, v133 wave_shl:1 row_mask:0xf bank_mask:0xf bound_ctrl:1
	v_pk_add_f32 v[62:63], v[30:31], v[120:121]
	v_pk_add_f32 v[30:31], v[50:51], v[122:123]
	v_pk_add_f32 v[50:51], v[60:61], v[126:127]
	v_pk_add_f32 v[60:61], v[64:65], v[130:131]
	v_pk_add_f32 v[64:65], v[82:83], v[132:133]
	v_mul_f32_e64 v140, v62, v22
	v_mul_f32_e64 v141, v63, v22
	v_mul_f32_e64 v142, v30, v22
	v_fma_f32 v29, v31, v22, v26
	v_mul_f32_e64 v52, v50, v22
	v_mul_f32_e64 v82, v51, v22
	v_fma_f32 v83, v60, v22, v26
	v_mul_f32_e64 v92, v61, v22
	v_fma_f32 v93, v64, v22, v26
	v_fma_f32 v29, -v140, v140, v29
	v_fma_f32 v52, -v140, v141, v52
	v_fma_f32 v82, -v140, v142, v82
	v_fma_f32 v83, -v141, v141, v83
	v_fma_f32 v92, -v141, v142, v92
	v_fma_f32 v93, -v142, v142, v93
	v_mul_f32_e64 v110, v92, v92
	v_mul_f32_e64 v111, v52, v93
	v_mul_f32_e64 v156, v82, v83
	v_mul_f32_e64 v157, v82, v82
	v_mul_f32_e64 v158, v29, v92
	v_mul_f32_e64 v159, v52, v52
	v_fma_f32 v110, v83, v93, -v110
	v_fma_f32 v111, v82, v92, -v111
	v_fma_f32 v156, v52, v92, -v156
	v_fma_f32 v157, v29, v93, -v157
	v_fma_f32 v158, v52, v82, -v158
	v_fma_f32 v159, v29, v83, -v159
	v_mul_f32_e64 v160, v29, v110
	v_fma_f32 v160, v52, v111, v160
	v_fma_f32 v160, v82, v156, v160
	v_rcp_f32_e32 v160, v160
	v_cmp_ne_u32_e64 vcc, s37, v25
	v_mul_f32_e64 v160, v160, v22
	v_cndmask_b32_e64 v160, 0, v160, s[30:31]
	v_cndmask_b32_e64 v29, 0, v18, vcc
	v_cndmask_b32_e64 v149, 0, v22, s[30:31]
	v_mul_f32_e64 v143, v110, v160
	v_mul_f32_e64 v144, v111, v160
	v_mul_f32_e64 v145, v156, v160
	v_mul_f32_e64 v146, v157, v160
	v_mul_f32_e64 v147, v158, v160
	v_mul_f32_e64 v148, v159, v160
	v_add_f32_e64 v150, v65, v29
	v_mov_b32_e32 v151, v25
	ds_write_b128 v23, v[140:143] offset:3072
	ds_write_b128 v23, v[144:147] offset:4096
	ds_write_b128 v23, v[148:151] offset:5120
	s_waitcnt lgkmcnt(0)
	s_barrier
	v_mov_b32_dpp v30, v6 wave_shr:1 row_mask:0xf bank_mask:0xf bound_ctrl:1
	v_mov_b32_dpp v31, v7 wave_shr:1 row_mask:0xf bank_mask:0xf bound_ctrl:1
	v_mov_b32_dpp v50, v6 wave_shl:1 row_mask:0xf bank_mask:0xf bound_ctrl:1
	v_mov_b32_dpp v51, v7 wave_shl:1 row_mask:0xf bank_mask:0xf bound_ctrl:1
	v_pk_mul_f32 v[60:61], v[6:7], v[12:13] op_sel_hi:[1,0]
	v_pk_mul_f32 v[62:63], v[6:7], v[12:13] op_sel:[0,1]
	v_pk_mul_f32 v[64:65], v[6:7], v[14:15] op_sel_hi:[1,0]
	v_pk_add_f32 v[82:83], v[6:7], v[30:31]
	v_pk_fma_f32 v[60:61], v[30:31], v[96:97], v[60:61] op_sel_hi:[1,0,1]
	v_pk_fma_f32 v[62:63], v[30:31], v[96:97], v[62:63] op_sel:[0,1,0]
	v_pk_fma_f32 v[64:65], v[30:31], v[98:99], v[64:65] op_sel_hi:[1,0,1]
	v_pk_add_f32 v[82:83], v[82:83], v[50:51]
	v_pk_fma_f32 v[60:61], v[50:51], v[100:101], v[60:61] op_sel_hi:[1,0,1]
	v_pk_fma_f32 v[62:63], v[50:51], v[100:101], v[62:63] op_sel:[0,1,0]
	v_pk_fma_f32 v[64:65], v[50:51], v[102:103], v[64:65] op_sel_hi:[1,0,1]
	v_pk_add_f32 v[30:31], v[38:39], v[82:83]
	v_pk_add_f32 v[38:39], v[94:95], v[60:61]
	v_pk_add_f32 v[50:51], v[56:57], v[62:63]
	v_pk_add_f32 v[56:57], v[66:67], v[64:65]
	v_pk_fma_f32 v[38:39], v[140:141], v[30:31], v[38:39] op_sel_hi:[0,1,1] neg_lo:[1,0,0] neg_hi:[1,0,0]
	v_pk_fma_f32 v[50:51], v[140:141], v[30:31], v[50:51] op_sel:[1,0,0] neg_lo:[1,0,0] neg_hi:[1,0,0]
	v_pk_fma_f32 v[56:57], v[142:143], v[30:31], v[56:57] op_sel_hi:[0,1,1] neg_lo:[1,0,0] neg_hi:[1,0,0]
	v_pk_mul_f32 v[66:67], v[142:143], v[38:39] op_sel:[1,0]
	v_pk_mul_f32 v[92:93], v[144:145], v[38:39] op_sel_hi:[0,1]
	v_pk_mul_f32 v[94:95], v[144:145], v[38:39] op_sel:[1,0]
	v_pk_fma_f32 v[66:67], v[144:145], v[50:51], v[66:67] op_sel_hi:[0,1,1]
	v_pk_fma_f32 v[92:93], v[146:147], v[50:51], v[92:93] op_sel_hi:[0,1,1]
	v_pk_fma_f32 v[94:95], v[146:147], v[50:51], v[94:95] op_sel:[1,0,0]
	v_pk_fma_f32 v[66:67], v[144:145], v[56:57], v[66:67] op_sel:[1,0,0]
	v_pk_fma_f32 v[92:93], v[146:147], v[56:57], v[92:93] op_sel:[1,0,0]
	v_pk_fma_f32 v[94:95], v[148:149], v[56:57], v[94:95] op_sel_hi:[0,1,1]
	v_pk_mul_f32 v[110:111], v[140:141], v[66:67] op_sel_hi:[0,1]
	v_pk_fma_f32 v[110:111], v[140:141], v[92:93], v[110:111] op_sel:[1,0,0]
	v_pk_fma_f32 v[110:111], v[142:143], v[94:95], v[110:111] op_sel_hi:[0,1,1]
	v_pk_fma_f32 v[110:111], v[148:149], v[30:31], v[110:111] op_sel:[1,0,0] neg_lo:[0,0,1] neg_hi:[0,0,1]
	v_cmp_eq_u32_e64 s[10:11], 6, v151
	v_cmp_eq_u32_e64 s[14:15], 7, v151
	v_pk_add_f32 v[30:31], v[58:59], v[66:67]
	v_pk_add_f32 v[38:39], v[88:89], v[92:93]
	v_pk_add_f32 v[50:51], v[108:109], v[94:95]
	v_pk_add_f32 v[56:57], v[118:119], v[110:111]
	v_pk_fma_f32 v[58:59], v[44:45], v[30:31], v[56:57] op_sel_hi:[0,1,1]
	v_pk_fma_f32 v[88:89], v[68:69], v[30:31], v[56:57] op_sel_hi:[0,1,1]
	v_pk_fma_f32 v[58:59], v[44:45], v[38:39], v[58:59] op_sel:[1,0,0]
	v_pk_fma_f32 v[88:89], v[68:69], v[38:39], v[88:89] op_sel:[1,0,0]
	v_pk_fma_f32 v[58:59], v[46:47], v[50:51], v[58:59] op_sel_hi:[0,1,1]
	v_pk_fma_f32 v[88:89], v[70:71], v[50:51], v[88:89] op_sel_hi:[0,1,1]
	v_pk_fma_f32 v[56:57], v[72:73], v[30:31], v[56:57] op_sel_hi:[0,1,1]
	v_pk_fma_f32 v[56:57], v[72:73], v[38:39], v[56:57] op_sel:[1,0,0]
	v_pk_fma_f32 v[56:57], v[74:75], v[50:51], v[56:57] op_sel_hi:[0,1,1]
	v_cndmask_b32_e64 v108, 0, v18, s[10:11]
	v_cndmask_b32_e64 v109, 0, v18, s[14:15]
	v_add_f32_dpp v56, v58, v56 wave_shl:1 row_mask:0xf bank_mask:0xf bound_ctrl:1
	v_add_f32_dpp v57, v59, v57 wave_shl:1 row_mask:0xf bank_mask:0xf bound_ctrl:1
	s_add_i32 s4, s34, 7
	s_cmpk_lt_i32 s4, 0x201
	s_cselect_b64 s[12:13], s[0:1], 0
	v_add_f32_dpp v56, v88, v56 wave_shr:1 row_mask:0xf bank_mask:0xf bound_ctrl:1
	v_add_f32_dpp v57, v89, v57 wave_shr:1 row_mask:0xf bank_mask:0xf bound_ctrl:1
	v_pk_fma_f32 v[56:57], v[48:49], v[150:151], v[56:57] op_sel_hi:[1,0,1] neg_lo:[0,0,1] neg_hi:[0,0,1]
	v_pk_add_f32 v[56:57], v[56:57], v[108:109] neg_lo:[0,1] neg_hi:[0,1]
	v_pk_mul_f32 v[118:119], v[56:57], v[56:57]
	v_add_f32_e32 v118, v118, v119
	v_cndmask_b32_e64 v119, 0, v118, s[12:13]
	v_add_f32_e32 v1, v1, v119
	s_waitcnt vmcnt(4)
	v_mov_b32_dpp v44, v32 wave_shr:1 row_mask:0xf bank_mask:0xf bound_ctrl:1
	v_mov_b32_dpp v45, v33 wave_shr:1 row_mask:0xf bank_mask:0xf bound_ctrl:1
	v_mov_b32_dpp v46, v34 wave_shr:1 row_mask:0xf bank_mask:0xf bound_ctrl:1
	v_mov_b32_dpp v48, v32 wave_shl:1 row_mask:0xf bank_mask:0xf bound_ctrl:1
	v_mov_b32_dpp v49, v33 wave_shl:1 row_mask:0xf bank_mask:0xf bound_ctrl:1
	v_mov_b32_dpp v50, v34 wave_shl:1 row_mask:0xf bank_mask:0xf bound_ctrl:1
	s_add_i32 s4, s34, 11
	s_cmpk_lt_u32 s4, 0x201
	s_cselect_b64 s[12:13], s[40:41], 0
	v_cmp_eq_u32_e64 s[14:15], s37, v3
	s_and_b64 s[14:15], s[14:15], s[12:13]
	v_cndmask_b32_e64 v25, 0, 1, s[14:15]
	v_mul_f32_e64 v30, v32, v32
	v_mul_f32_e64 v31, v32, v33
	v_mul_f32_e64 v38, v32, v34
	v_mul_f32_e64 v39, v33, v33
	v_mul_f32_e64 v56, v33, v34
	v_mul_f32_e64 v57, v34, v34
	v_or_b32_dpp v29, v25, v25 wave_shr:1 row_mask:0xf bank_mask:0xf bound_ctrl:1
	s_nop 1
	v_or_b32_dpp v29, v25, v29 wave_shl:1 row_mask:0xf bank_mask:0xf bound_ctrl:1
	s_nop 1
	v_or_b32_dpp v52, v29, v29 wave_shr:1 row_mask:0xf bank_mask:0xf bound_ctrl:1
	s_nop 1
	v_or_b32_dpp v52, v29, v52 wave_shl:1 row_mask:0xf bank_mask:0xf bound_ctrl:1
	v_or3_b32 v25, v52, v85, v128
	v_or3_b32 v25, v25, v129, v53
	s_add_i32 s4, s34, 8
	s_cmpk_lt_u32 s4, 0x1ff
	s_cselect_b64 s[12:13], s[42:43], 0
	v_cmp_ne_u32_e64 s[30:31], 0, v25
	s_and_b64 s[30:31], s[30:31], s[12:13]
	v_cndmask_b32_e64 v25, 0, 1.0, s[30:31]
	v_add_f32_e64 v58, v32, v44
	v_add_f32_e64 v59, v33, v45
	v_add_f32_e64 v68, v34, v46
	v_fma_f32 v30, v44, v44, v30
	v_fma_f32 v31, v44, v45, v31
	v_fma_f32 v38, v44, v46, v38
	v_fma_f32 v39, v45, v45, v39
	v_fma_f32 v56, v45, v46, v56
	v_fma_f32 v57, v46, v46, v57
	v_add_f32_dpp v75, v25, v25 wave_shr:1 row_mask:0xf bank_mask:0xf bound_ctrl:1
	v_add_f32_e64 v58, v58, v48
	v_add_f32_e64 v59, v59, v49
	v_add_f32_e64 v68, v68, v50
	v_fma_f32 v69, v48, v48, v30
	v_fma_f32 v70, v48, v49, v31
	v_fma_f32 v71, v48, v50, v38
	v_fma_f32 v72, v49, v49, v39
	v_fma_f32 v73, v49, v50, v56
	v_fma_f32 v74, v50, v50, v57
	v_add_f32_dpp v75, v25, v75 wave_shl:1 row_mask:0xf bank_mask:0xf bound_ctrl:1
	v_pk_add_f32 v[30:31], v[120:121], v[58:59]
	v_pk_add_f32 v[38:39], v[54:55], v[30:31]
	v_pk_add_f32 v[54:55], v[122:123], v[68:69]
	v_pk_add_f32 v[56:57], v[80:81], v[54:55]
	v_pk_add_f32 v[80:81], v[126:127], v[70:71]
	v_pk_add_f32 v[88:89], v[90:91], v[80:81]
	v_pk_add_f32 v[90:91], v[130:131], v[72:73]
	v_pk_add_f32 v[108:109], v[116:117], v[90:91]
	v_pk_add_f32 v[116:117], v[132:133], v[74:75]
	v_pk_add_f32 v[118:119], v[124:125], v[116:117]
	v_mul_f32_e64 v120, v38, v22
	v_mul_f32_e64 v121, v39, v22
	v_mul_f32_e64 v122, v56, v22
	v_fma_f32 v25, v57, v22, v26
	v_mul_f32_e64 v29, v88, v22
	v_mul_f32_e64 v84, v89, v22
	v_fma_f32 v130, v108, v22, v26
	v_mul_f32_e64 v131, v109, v22
	v_fma_f32 v132, v118, v22, v26
	v_fma_f32 v25, -v120, v120, v25
	v_fma_f32 v29, -v120, v121, v29
	v_fma_f32 v84, -v120, v122, v84
	v_fma_f32 v130, -v121, v121, v130
	v_fma_f32 v131, -v121, v122, v131
	v_fma_f32 v132, -v122, v122, v132
	v_mul_f32_e64 v133, v131, v131
	v_mul_f32_e64 v144, v29, v132
	v_mul_f32_e64 v145, v84, v130
	v_mul_f32_e64 v146, v84, v84
	v_mul_f32_e64 v147, v25, v131
	v_mul_f32_e64 v148, v29, v29
	v_fma_f32 v133, v130, v132, -v133
	v_fma_f32 v144, v84, v131, -v144
	v_fma_f32 v145, v29, v131, -v145
	v_fma_f32 v146, v25, v132, -v146
	v_fma_f32 v147, v29, v84, -v147
	v_fma_f32 v148, v25, v130, -v148
	v_mul_f32_e64 v149, v25, v133
	v_fma_f32 v149, v29, v144, v149
	v_fma_f32 v149, v84, v145, v149
	v_rcp_f32_e32 v149, v149
	v_cmp_ne_u32_e64 vcc, s37, v24
	v_mul_f32_e64 v149, v149, v22
	v_cndmask_b32_e64 v149, 0, v149, s[30:31]
	v_cndmask_b32_e64 v25, 0, v18, vcc
	v_cndmask_b32_e64 v141, 0, v22, s[30:31]
	v_mul_f32_e64 v123, v133, v149
	v_mul_f32_e64 v124, v144, v149
	v_mul_f32_e64 v125, v145, v149
	v_mul_f32_e64 v126, v146, v149
	v_mul_f32_e64 v127, v147, v149
	v_mul_f32_e64 v140, v148, v149
	v_add_f32_e64 v142, v119, v25
	v_mov_b32_e32 v143, v24
	ds_write_b128 v23, v[120:123]
	ds_write_b128 v23, v[124:127] offset:1024
	ds_write_b128 v23, v[140:143] offset:2048
	s_waitcnt lgkmcnt(0)
	s_barrier
	v_mov_b32_dpp v24, v20 wave_shr:1 row_mask:0xf bank_mask:0xf bound_ctrl:1
	v_mov_b32_dpp v25, v21 wave_shr:1 row_mask:0xf bank_mask:0xf bound_ctrl:1
	v_mov_b32_dpp v38, v20 wave_shl:1 row_mask:0xf bank_mask:0xf bound_ctrl:1
	v_mov_b32_dpp v39, v21 wave_shl:1 row_mask:0xf bank_mask:0xf bound_ctrl:1
	v_pk_mul_f32 v[56:57], v[20:21], v[32:33] op_sel_hi:[1,0]
	v_pk_mul_f32 v[88:89], v[20:21], v[32:33] op_sel:[0,1]
	v_pk_mul_f32 v[108:109], v[20:21], v[34:35] op_sel_hi:[1,0]
	v_pk_add_f32 v[118:119], v[20:21], v[24:25]
	v_pk_fma_f32 v[56:57], v[24:25], v[44:45], v[56:57] op_sel_hi:[1,0,1]
	v_pk_fma_f32 v[88:89], v[24:25], v[44:45], v[88:89] op_sel:[0,1,0]
	v_pk_fma_f32 v[108:109], v[24:25], v[46:47], v[108:109] op_sel_hi:[1,0,1]
	v_pk_add_f32 v[118:119], v[118:119], v[38:39]
	v_pk_fma_f32 v[56:57], v[38:39], v[48:49], v[56:57] op_sel_hi:[1,0,1]
	v_pk_fma_f32 v[88:89], v[38:39], v[48:49], v[88:89] op_sel:[0,1,0]
	v_pk_fma_f32 v[108:109], v[38:39], v[50:51], v[108:109] op_sel_hi:[1,0,1]
	v_pk_add_f32 v[24:25], v[82:83], v[118:119]
	v_pk_add_f32 v[38:39], v[138:139], v[24:25]
	v_pk_add_f32 v[82:83], v[60:61], v[56:57]
	v_pk_add_f32 v[130:131], v[112:113], v[82:83]
	v_pk_add_f32 v[60:61], v[62:63], v[88:89]
	v_pk_add_f32 v[112:113], v[134:135], v[60:61]
	v_pk_add_f32 v[62:63], v[64:65], v[108:109]
	v_pk_add_f32 v[132:133], v[136:137], v[62:63]
	v_pk_fma_f32 v[130:131], v[120:121], v[38:39], v[130:131] op_sel_hi:[0,1,1] neg_lo:[1,0,0] neg_hi:[1,0,0]
	v_pk_fma_f32 v[112:113], v[120:121], v[38:39], v[112:113] op_sel:[1,0,0] neg_lo:[1,0,0] neg_hi:[1,0,0]
	v_pk_fma_f32 v[132:133], v[122:123], v[38:39], v[132:133] op_sel_hi:[0,1,1] neg_lo:[1,0,0] neg_hi:[1,0,0]
	v_pk_mul_f32 v[64:65], v[122:123], v[130:131] op_sel:[1,0]
	v_pk_mul_f32 v[134:135], v[124:125], v[130:131] op_sel_hi:[0,1]
	v_pk_mul_f32 v[136:137], v[124:125], v[130:131] op_sel:[1,0]
	v_pk_fma_f32 v[64:65], v[124:125], v[112:113], v[64:65] op_sel_hi:[0,1,1]
	v_pk_fma_f32 v[134:135], v[126:127], v[112:113], v[134:135] op_sel_hi:[0,1,1]
	v_pk_fma_f32 v[136:137], v[126:127], v[112:113], v[136:137] op_sel:[1,0,0]
	v_pk_fma_f32 v[64:65], v[124:125], v[132:133], v[64:65] op_sel:[1,0,0]
	v_pk_fma_f32 v[134:135], v[126:127], v[132:133], v[134:135] op_sel:[1,0,0]
	v_pk_fma_f32 v[136:137], v[140:141], v[132:133], v[136:137] op_sel_hi:[0,1,1]
	v_pk_mul_f32 v[138:139], v[120:121], v[64:65] op_sel_hi:[0,1]
	v_pk_fma_f32 v[138:139], v[120:121], v[134:135], v[138:139] op_sel:[1,0,0]
	v_pk_fma_f32 v[138:139], v[122:123], v[136:137], v[138:139] op_sel_hi:[0,1,1]
	v_pk_fma_f32 v[138:139], v[140:141], v[38:39], v[138:139] op_sel:[1,0,0] neg_lo:[0,0,1] neg_hi:[0,0,1]
	v_cmp_eq_u32_e64 s[10:11], 6, v143
	v_cmp_eq_u32_e64 s[14:15], 7, v143
	v_pk_add_f32 v[38:39], v[66:67], v[64:65]
	v_pk_add_f32 v[112:113], v[86:87], v[38:39]
	v_pk_add_f32 v[66:67], v[92:93], v[134:135]
	v_pk_add_f32 v[86:87], v[114:115], v[66:67]
	v_pk_add_f32 v[92:93], v[94:95], v[136:137]
	v_pk_add_f32 v[114:115], v[152:153], v[92:93]
	v_pk_add_f32 v[94:95], v[110:111], v[138:139]
	v_pk_add_f32 v[130:131], v[154:155], v[94:95]
	v_pk_fma_f32 v[110:111], v[76:77], v[112:113], v[130:131] op_sel_hi:[0,1,1]
	v_pk_fma_f32 v[132:133], v[104:105], v[112:113], v[130:131] op_sel_hi:[0,1,1]
	v_pk_fma_f32 v[110:111], v[76:77], v[86:87], v[110:111] op_sel:[1,0,0]
	v_pk_fma_f32 v[132:133], v[104:105], v[86:87], v[132:133] op_sel:[1,0,0]
	v_pk_fma_f32 v[110:111], v[78:79], v[114:115], v[110:111] op_sel_hi:[0,1,1]
	v_pk_fma_f32 v[132:133], v[106:107], v[114:115], v[132:133] op_sel_hi:[0,1,1]
	v_pk_fma_f32 v[130:131], v[8:9], v[112:113], v[130:131] op_sel_hi:[0,1,1]
	v_pk_fma_f32 v[130:131], v[8:9], v[86:87], v[130:131] op_sel:[1,0,0]
	v_pk_fma_f32 v[130:131], v[10:11], v[114:115], v[130:131] op_sel_hi:[0,1,1]
	v_cndmask_b32_e64 v144, 0, v18, s[10:11]
	v_cndmask_b32_e64 v145, 0, v18, s[14:15]
	v_add_f32_dpp v130, v110, v130 wave_shl:1 row_mask:0xf bank_mask:0xf bound_ctrl:1
	v_add_f32_dpp v131, v111, v131 wave_shl:1 row_mask:0xf bank_mask:0xf bound_ctrl:1
	s_add_i32 s4, s34, 8
	s_cmpk_lt_i32 s4, 0x201
	s_cselect_b64 s[12:13], s[0:1], 0
	v_add_f32_dpp v130, v132, v130 wave_shr:1 row_mask:0xf bank_mask:0xf bound_ctrl:1
	v_add_f32_dpp v131, v133, v131 wave_shr:1 row_mask:0xf bank_mask:0xf bound_ctrl:1
	v_pk_fma_f32 v[130:131], v[4:5], v[142:143], v[130:131] op_sel_hi:[1,0,1] neg_lo:[0,0,1] neg_hi:[0,0,1]
	v_pk_add_f32 v[130:131], v[130:131], v[144:145] neg_lo:[0,1] neg_hi:[0,1]
	v_pk_mul_f32 v[146:147], v[130:131], v[130:131]
	v_add_f32_e32 v146, v146, v147
	v_cndmask_b32_e64 v147, 0, v146, s[12:13]
	v_add_f32_e32 v1, v1, v147
	s_waitcnt vmcnt(0)
	v_mov_b32_dpp v8, v40 wave_shr:1 row_mask:0xf bank_mask:0xf bound_ctrl:1
	v_mov_b32_dpp v9, v41 wave_shr:1 row_mask:0xf bank_mask:0xf bound_ctrl:1
	v_mov_b32_dpp v10, v42 wave_shr:1 row_mask:0xf bank_mask:0xf bound_ctrl:1
	v_mov_b32_dpp v76, v40 wave_shl:1 row_mask:0xf bank_mask:0xf bound_ctrl:1
	v_mov_b32_dpp v77, v41 wave_shl:1 row_mask:0xf bank_mask:0xf bound_ctrl:1
	v_mov_b32_dpp v78, v42 wave_shl:1 row_mask:0xf bank_mask:0xf bound_ctrl:1
	s_add_i32 s4, s34, 12
	s_cmpk_lt_u32 s4, 0x201
	s_cselect_b64 s[12:13], s[40:41], 0
	v_cmp_eq_u32_e64 s[14:15], s37, v16
	s_and_b64 s[14:15], s[14:15], s[12:13]
	v_cndmask_b32_e64 v29, 0, 1, s[14:15]
	v_mul_f32_e64 v4, v40, v40
	v_mul_f32_e64 v5, v40, v41
	v_mul_f32_e64 v86, v40, v42
	v_mul_f32_e64 v87, v41, v41
	v_mul_f32_e64 v104, v41, v42
	v_mul_f32_e64 v105, v42, v42
	v_or_b32_dpp v53, v29, v29 wave_shr:1 row_mask:0xf bank_mask:0xf bound_ctrl:1
	s_nop 1
	v_or_b32_dpp v53, v29, v53 wave_shl:1 row_mask:0xf bank_mask:0xf bound_ctrl:1
	s_nop 1
	v_or_b32_dpp v84, v53, v53 wave_shr:1 row_mask:0xf bank_mask:0xf bound_ctrl:1
	s_nop 1
	v_or_b32_dpp v84, v53, v84 wave_shl:1 row_mask:0xf bank_mask:0xf bound_ctrl:1
	v_or3_b32 v29, v84, v52, v85
	v_or3_b32 v29, v29, v128, v129
	s_add_i32 s4, s34, 9
	s_cmpk_lt_u32 s4, 0x1ff
	s_cselect_b64 s[12:13], s[42:43], 0
	v_cmp_ne_u32_e64 s[30:31], 0, v29
	s_and_b64 s[30:31], s[30:31], s[12:13]
	v_cndmask_b32_e64 v29, 0, 1.0, s[30:31]
	v_add_f32_e64 v106, v40, v8
	v_add_f32_e64 v107, v41, v9
	v_add_f32_e64 v110, v42, v10
	v_fma_f32 v4, v8, v8, v4
	v_fma_f32 v5, v8, v9, v5
	v_fma_f32 v86, v8, v10, v86
	v_fma_f32 v87, v9, v9, v87
	v_fma_f32 v104, v9, v10, v104
	v_fma_f32 v105, v10, v10, v105
	v_add_f32_dpp v121, v29, v29 wave_shr:1 row_mask:0xf bank_mask:0xf bound_ctrl:1
	v_add_f32_e64 v106, v106, v76
	v_add_f32_e64 v107, v107, v77
	v_add_f32_e64 v110, v110, v78
	v_fma_f32 v111, v76, v76, v4
	v_fma_f32 v112, v76, v77, v5
	v_fma_f32 v113, v76, v78, v86
	v_fma_f32 v114, v77, v77, v87
	v_fma_f32 v115, v77, v78, v104
	v_fma_f32 v120, v78, v78, v105
	v_add_f32_dpp v121, v29, v121 wave_shl:1 row_mask:0xf bank_mask:0xf bound_ctrl:1
	v_pk_add_f32 v[4:5], v[30:31], v[106:107]
	v_pk_add_f32 v[30:31], v[54:55], v[110:111]
	v_pk_add_f32 v[54:55], v[80:81], v[112:113]
	v_pk_add_f32 v[80:81], v[90:91], v[114:115]
	v_pk_add_f32 v[86:87], v[116:117], v[120:121]
	v_mul_f32_e64 v124, v4, v22
	v_mul_f32_e64 v125, v5, v22
	v_mul_f32_e64 v126, v30, v22
	v_fma_f32 v29, v31, v22, v26
	v_mul_f32_e64 v53, v54, v22
	v_mul_f32_e64 v90, v55, v22
	v_fma_f32 v91, v80, v22, v26
	v_mul_f32_e64 v104, v81, v22
	v_fma_f32 v105, v86, v22, v26
	v_fma_f32 v29, -v124, v124, v29
	v_fma_f32 v53, -v124, v125, v53
	v_fma_f32 v90, -v124, v126, v90
	v_fma_f32 v91, -v125, v125, v91
	v_fma_f32 v104, -v125, v126, v104
	v_fma_f32 v105, -v126, v126, v105
	v_mul_f32_e64 v116, v104, v104
	v_mul_f32_e64 v117, v53, v105
	v_mul_f32_e64 v122, v90, v91
	v_mul_f32_e64 v123, v90, v90
	v_mul_f32_e64 v130, v29, v104
	v_mul_f32_e64 v131, v53, v53
	v_fma_f32 v116, v91, v105, -v116
	v_fma_f32 v117, v90, v104, -v117
	v_fma_f32 v122, v53, v104, -v122
	v_fma_f32 v123, v29, v105, -v123
	v_fma_f32 v130, v53, v90, -v130
	v_fma_f32 v131, v29, v91, -v131
	v_mul_f32_e64 v132, v29, v116
	v_fma_f32 v132, v53, v117, v132
	v_fma_f32 v132, v90, v122, v132
	v_rcp_f32_e32 v132, v132
	v_cmp_ne_u32_e64 vcc, s37, v17
	v_mul_f32_e64 v132, v132, v22
	v_cndmask_b32_e64 v132, 0, v132, s[30:31]
	v_cndmask_b32_e64 v29, 0, v18, vcc
	v_cndmask_b32_e64 v145, 0, v22, s[30:31]
	v_mul_f32_e64 v127, v116, v132
	v_mul_f32_e64 v140, v117, v132
	v_mul_f32_e64 v141, v122, v132
	v_mul_f32_e64 v142, v123, v132
	v_mul_f32_e64 v143, v130, v132
	v_mul_f32_e64 v144, v131, v132
	v_add_f32_e64 v146, v87, v29
	v_mov_b32_e32 v147, v17
	ds_write_b128 v23, v[124:127] offset:3072
	ds_write_b128 v23, v[140:143] offset:4096
	ds_write_b128 v23, v[144:147] offset:5120
	s_waitcnt lgkmcnt(0)
	s_barrier
	v_mov_b32_dpp v4, v36 wave_shr:1 row_mask:0xf bank_mask:0xf bound_ctrl:1
	v_mov_b32_dpp v5, v37 wave_shr:1 row_mask:0xf bank_mask:0xf bound_ctrl:1
	v_mov_b32_dpp v30, v36 wave_shl:1 row_mask:0xf bank_mask:0xf bound_ctrl:1
	v_mov_b32_dpp v31, v37 wave_shl:1 row_mask:0xf bank_mask:0xf bound_ctrl:1
	v_pk_mul_f32 v[54:55], v[36:37], v[40:41] op_sel_hi:[1,0]
	v_pk_mul_f32 v[80:81], v[36:37], v[40:41] op_sel:[0,1]
	v_pk_mul_f32 v[86:87], v[36:37], v[42:43] op_sel_hi:[1,0]
	v_pk_add_f32 v[90:91], v[36:37], v[4:5]
	v_pk_fma_f32 v[54:55], v[4:5], v[8:9], v[54:55] op_sel_hi:[1,0,1]
	v_pk_fma_f32 v[80:81], v[4:5], v[8:9], v[80:81] op_sel:[0,1,0]
	v_pk_fma_f32 v[86:87], v[4:5], v[10:11], v[86:87] op_sel_hi:[1,0,1]
	v_pk_add_f32 v[90:91], v[90:91], v[30:31]
	v_pk_fma_f32 v[54:55], v[30:31], v[76:77], v[54:55] op_sel_hi:[1,0,1]
	v_pk_fma_f32 v[80:81], v[30:31], v[76:77], v[80:81] op_sel:[0,1,0]
	v_pk_fma_f32 v[86:87], v[30:31], v[78:79], v[86:87] op_sel_hi:[1,0,1]
	v_pk_add_f32 v[4:5], v[24:25], v[90:91]
	v_pk_add_f32 v[24:25], v[82:83], v[54:55]
	v_pk_add_f32 v[30:31], v[60:61], v[80:81]
	v_pk_add_f32 v[60:61], v[62:63], v[86:87]
	v_pk_fma_f32 v[24:25], v[124:125], v[4:5], v[24:25] op_sel_hi:[0,1,1] neg_lo:[1,0,0] neg_hi:[1,0,0]
	v_pk_fma_f32 v[30:31], v[124:125], v[4:5], v[30:31] op_sel:[1,0,0] neg_lo:[1,0,0] neg_hi:[1,0,0]
	v_pk_fma_f32 v[60:61], v[126:127], v[4:5], v[60:61] op_sel_hi:[0,1,1] neg_lo:[1,0,0] neg_hi:[1,0,0]
	v_pk_mul_f32 v[62:63], v[126:127], v[24:25] op_sel:[1,0]
	v_pk_mul_f32 v[82:83], v[140:141], v[24:25] op_sel_hi:[0,1]
	v_pk_mul_f32 v[104:105], v[140:141], v[24:25] op_sel:[1,0]
	v_pk_fma_f32 v[62:63], v[140:141], v[30:31], v[62:63] op_sel_hi:[0,1,1]
	v_pk_fma_f32 v[82:83], v[142:143], v[30:31], v[82:83] op_sel_hi:[0,1,1]
	v_pk_fma_f32 v[104:105], v[142:143], v[30:31], v[104:105] op_sel:[1,0,0]
	v_pk_fma_f32 v[62:63], v[140:141], v[60:61], v[62:63] op_sel:[1,0,0]
	v_pk_fma_f32 v[82:83], v[142:143], v[60:61], v[82:83] op_sel:[1,0,0]
	v_pk_fma_f32 v[104:105], v[144:145], v[60:61], v[104:105] op_sel_hi:[0,1,1]
	v_pk_mul_f32 v[116:117], v[124:125], v[62:63] op_sel_hi:[0,1]
	v_pk_fma_f32 v[116:117], v[124:125], v[82:83], v[116:117] op_sel:[1,0,0]
	v_pk_fma_f32 v[116:117], v[126:127], v[104:105], v[116:117] op_sel_hi:[0,1,1]
	v_pk_fma_f32 v[116:117], v[144:145], v[4:5], v[116:117] op_sel:[1,0,0] neg_lo:[0,0,1] neg_hi:[0,0,1]
	v_cmp_eq_u32_e64 s[10:11], 6, v147
	v_cmp_eq_u32_e64 s[14:15], 7, v147
	v_pk_add_f32 v[4:5], v[38:39], v[62:63]
	v_pk_add_f32 v[24:25], v[66:67], v[82:83]
	v_pk_add_f32 v[30:31], v[92:93], v[104:105]
	v_pk_add_f32 v[38:39], v[94:95], v[116:117]
	v_pk_fma_f32 v[60:61], v[96:97], v[4:5], v[38:39] op_sel_hi:[0,1,1]
	v_pk_fma_f32 v[66:67], v[100:101], v[4:5], v[38:39] op_sel_hi:[0,1,1]
	v_pk_fma_f32 v[60:61], v[96:97], v[24:25], v[60:61] op_sel:[1,0,0]
	v_pk_fma_f32 v[66:67], v[100:101], v[24:25], v[66:67] op_sel:[1,0,0]
	v_pk_fma_f32 v[60:61], v[98:99], v[30:31], v[60:61] op_sel_hi:[0,1,1]
	v_pk_fma_f32 v[66:67], v[102:103], v[30:31], v[66:67] op_sel_hi:[0,1,1]
	v_pk_fma_f32 v[38:39], v[12:13], v[4:5], v[38:39] op_sel_hi:[0,1,1]
	v_pk_fma_f32 v[38:39], v[12:13], v[24:25], v[38:39] op_sel:[1,0,0]
	v_pk_fma_f32 v[38:39], v[14:15], v[30:31], v[38:39] op_sel_hi:[0,1,1]
	v_cndmask_b32_e64 v92, 0, v18, s[10:11]
	v_cndmask_b32_e64 v93, 0, v18, s[14:15]
	v_add_f32_dpp v38, v60, v38 wave_shl:1 row_mask:0xf bank_mask:0xf bound_ctrl:1
	v_add_f32_dpp v39, v61, v39 wave_shl:1 row_mask:0xf bank_mask:0xf bound_ctrl:1
	s_add_i32 s4, s34, 9
	s_cmpk_lt_i32 s4, 0x201
	s_cselect_b64 s[12:13], s[0:1], 0
	v_add_f32_dpp v38, v66, v38 wave_shr:1 row_mask:0xf bank_mask:0xf bound_ctrl:1
	v_add_f32_dpp v39, v67, v39 wave_shr:1 row_mask:0xf bank_mask:0xf bound_ctrl:1
	v_pk_fma_f32 v[38:39], v[6:7], v[146:147], v[38:39] op_sel_hi:[1,0,1] neg_lo:[0,0,1] neg_hi:[0,0,1]
	v_pk_add_f32 v[38:39], v[38:39], v[92:93] neg_lo:[0,1] neg_hi:[0,1]
	v_pk_mul_f32 v[94:95], v[38:39], v[38:39]
	v_add_f32_e32 v94, v94, v95
	v_cndmask_b32_e64 v95, 0, v94, s[12:13]
	v_add_f32_e32 v1, v1, v95
	v_mov_b32_e32 v0, v1
	s_branch .LBB0_29
